# route: all sixteen row loads of the next round prefetched after the last router MFMA (five through staging registers copied where the late loads were); stacked
# baseline (speedup 1.0000x reference)
.LBB0_587:
	s_and_saveexec_b64 s[6:7], s[10:11]
	ds_write_b32 v219, v125
	s_or_b64 exec, exec, s[6:7]
	s_lshl_b32 s66, s93, 6
	s_add_i32 s67, s66, s2
	s_mov_b32 s68, 0
	s_waitcnt lgkmcnt(0)
	s_barrier
	s_mov_b32 s82, 0
	s_lshl_b32 s82, s82, 4
	s_add_i32 s82, s67, s82
	s_ashr_i32 s83, s82, 31
	s_lshl_b64 s[82:83], s[82:83], 13
	v_lshl_add_u64 v[98:99], v[128:129], 0, s[82:83]
	s_add_u32 s82, s82, 0x1000
	s_addc_u32 s83, s83, 0
	global_load_dwordx4 v[118:121], v[98:99], off
	global_load_dwordx4 v[114:117], v[98:99], off offset:16
	global_load_dwordx4 v[110:113], v[98:99], off offset:2048
	global_load_dwordx4 v[106:109], v[98:99], off offset:2064
	v_lshl_add_u64 v[100:101], v[128:129], 0, s[82:83]
	s_add_u32 s82, s82, 0x1000
	s_addc_u32 s83, s83, 0
	global_load_dwordx4 v[58:61], v[100:101], off offset:2064
	global_load_dwordx4 v[90:93], v[100:101], off
	global_load_dwordx4 v[66:69], v[100:101], off offset:16
	global_load_dwordx4 v[62:65], v[100:101], off offset:2048
	v_lshl_add_u64 v[98:99], v[128:129], 0, s[82:83]
	s_nop 0
	global_load_dwordx4 v[54:57], v[98:99], off
	global_load_dwordx4 v[50:53], v[98:99], off offset:16
	global_load_dwordx4 v[234:237], v[98:99], off offset:2064
	global_load_dwordx4 v[238:241], v[98:99], off offset:2048
	s_add_u32 s82, s82, 0x1000
	s_addc_u32 s83, s83, 0
	v_lshl_add_u64 v[100:101], v[128:129], 0, s[82:83]
	s_nop 0
	global_load_dwordx4 v[242:245], v[100:101], off
	global_load_dwordx4 v[246:249], v[100:101], off offset:16
	global_load_dwordx4 v[102:105], v[100:101], off offset:2048
	global_load_dwordx4 v[250:253], v[100:101], off offset:2064
	s_branch .LBB0_592

.LBB0_592:
	s_lshl_b32 s8, s68, 4
	s_add_i32 s6, s67, s8
	s_ashr_i32 s7, s6, 31
	s_lshl_b64 s[12:13], s[6:7], 13
	v_lshl_add_u64 v[34:35], v[128:129], 0, s[12:13]
	v_lshl_add_u64 v[36:37], v[34:35], 0, s[48:49]
	v_add_co_u32_e32 v36, vcc, 0x1000, v34
	v_and_b32_e32 v1, 64, v220
	s_nop 0
	v_addc_co_u32_e32 v37, vcc, 0, v35, vcc
	v_lshl_add_u64 v[34:35], v[34:35], 0, s[46:47]
	v_xor_b32_e32 v34, 1, v220
	v_add_u32_e32 v1, 64, v1
	s_or_b32 s6, s6, 1
	v_cmp_lt_i32_e32 vcc, v34, v1
	s_ashr_i32 s7, s6, 31
	s_lshl_b64 s[6:7], s[6:7], 13
	v_cndmask_b32_e32 v34, v220, v34, vcc
	v_lshlrev_b32_e32 v218, 2, v34
	v_lshl_add_u64 v[34:35], v[128:129], 0, s[6:7]
	v_add_co_u32_e32 v70, vcc, s34, v34
	v_lshl_add_u64 v[36:37], v[34:35], 0, s[46:47]
	s_nop 0
	v_addc_co_u32_e32 v71, vcc, 0, v35, vcc
	v_lshl_add_u64 v[72:73], v[34:35], 0, s[48:49]
	s_nop 0
	s_add_i32 s8, s8, s66
	s_add_i32 s54, s8, s2
	s_ashr_i32 s55, s54, 31
	s_add_i32 s58, s8, s27
	s_ashr_i32 s59, s58, 31
	s_waitcnt vmcnt(13)
	v_mov_b32_e32 v76, v119
	s_waitcnt vmcnt(12)
	v_mov_b32_e32 v77, v115
	v_mov_b32_e32 v80, v121
	v_mov_b32_e32 v81, v117
	v_mov_b32_e32 v74, v118
	v_mov_b32_e32 v75, v114
	v_mov_b32_e32 v78, v120
	v_mov_b32_e32 v79, v116
	s_waitcnt vmcnt(11)
	v_pk_mul_f32 v[82:83], v[112:113], v[112:113]
	v_pk_mul_f32 v[84:85], v[110:111], v[110:111]
	v_pk_mul_f32 v[76:77], v[76:77], v[76:77]
	v_pk_mul_f32 v[80:81], v[80:81], v[80:81]
	v_pk_mov_b32 v[94:95], v[84:85], v[82:83] op_sel:[1,0]
	v_mov_b32_e32 v85, v83
	v_pk_fma_f32 v[74:75], v[74:75], v[74:75], v[76:77]
	v_pk_fma_f32 v[76:77], v[78:79], v[78:79], v[80:81]
	s_waitcnt vmcnt(10)
	v_mul_f32_e32 v86, v107, v107
	v_mul_f32_e32 v88, v109, v109
	v_pk_add_f32 v[78:79], v[94:95], v[84:85]
	v_pk_add_f32 v[74:75], v[74:75], v[76:77]
	v_pk_fma_f32 v[82:83], v[106:107], v[106:107], v[86:87] op_sel_hi:[1,1,0]
	v_pk_fma_f32 v[86:87], v[108:109], v[108:109], v[88:89] op_sel_hi:[1,1,0]
	s_waitcnt vmcnt(8)
	v_mul_f32_e32 v95, v90, v90
	v_mul_f32_e32 v100, v91, v91
	v_pk_add_f32 v[76:77], v[78:79], v[78:79] op_sel:[0,1] op_sel_hi:[1,0]
	v_pk_add_f32 v[74:75], v[74:75], v[74:75] op_sel:[0,1] op_sel_hi:[1,0]
	v_mul_f32_e32 v83, v92, v92
	v_mul_f32_e32 v87, v93, v93
	s_waitcnt vmcnt(7)
	v_pk_mul_f32 v[80:81], v[68:69], v[68:69]
	v_pk_mul_f32 v[84:85], v[66:67], v[66:67]
	v_mov_b32_e32 v77, v100
	v_mov_b32_e32 v75, v95
	v_pk_mov_b32 v[78:79], v[84:85], v[80:81] op_sel:[1,0]
	v_mov_b32_e32 v85, v81
	v_pk_add_f32 v[82:83], v[82:83], v[86:87]
	v_pk_add_f32 v[74:75], v[74:75], v[76:77]
	s_waitcnt vmcnt(6)
	v_mul_f32_e32 v88, v63, v63
	v_mul_f32_e32 v94, v65, v65
	v_pk_add_f32 v[78:79], v[78:79], v[84:85]
	v_pk_add_f32 v[74:75], v[74:75], v[82:83]
	v_mul_f32_e32 v96, v58, v58
	v_mul_f32_e32 v97, v59, v59
	v_mul_f32_e32 v98, v60, v60
	v_mul_f32_e32 v99, v61, v61
	v_pk_fma_f32 v[80:81], v[62:63], v[62:63], v[88:89] op_sel_hi:[1,1,0]
	v_pk_fma_f32 v[88:89], v[64:65], v[64:65], v[94:95] op_sel_hi:[1,1,0]
	v_pk_add_f32 v[78:79], v[78:79], v[78:79] op_sel:[0,1] op_sel_hi:[1,0]
	v_pk_add_f32 v[74:75], v[74:75], v[74:75] op_sel:[0,1] op_sel_hi:[1,0]
	v_mov_b32_e32 v81, v98
	v_mov_b32_e32 v79, v97
	v_mov_b32_e32 v75, v96
	v_mov_b32_e32 v89, v99
	v_pk_add_f32 v[74:75], v[74:75], v[78:79]
	v_pk_add_f32 v[76:77], v[80:81], v[88:89]
	s_waitcnt vmcnt(0)
	v_mov_b32_e32 v42, v234
	v_mov_b32_e32 v43, v235
	v_mov_b32_e32 v44, v236
	v_mov_b32_e32 v45, v237
	v_mov_b32_e32 v46, v238
	v_mov_b32_e32 v47, v239
	v_mov_b32_e32 v48, v240
	v_mov_b32_e32 v49, v241
	v_mov_b32_e32 v38, v242
	v_mov_b32_e32 v39, v243
	v_mov_b32_e32 v40, v244
	v_mov_b32_e32 v41, v245
	v_mov_b32_e32 v34, v246
	v_mov_b32_e32 v35, v247
	v_mov_b32_e32 v36, v248
	v_mov_b32_e32 v37, v249
	v_mov_b32_e32 v98, v250
	v_mov_b32_e32 v99, v251
	v_mov_b32_e32 v100, v252
	v_mov_b32_e32 v101, v253
	global_load_dwordx4 v[82:85], v[126:127], off
	global_load_dwordx4 v[86:89], v[126:127], off offset:256
	v_pk_add_f32 v[74:75], v[74:75], v[76:77]
	v_xor_b32_e32 v76, 2, v220
	v_add_f32_e32 v74, v74, v75
	ds_bpermute_b32 v75, v218, v74
	v_cmp_lt_i32_e32 vcc, v76, v1
	s_waitcnt lgkmcnt(0)
	v_add_f32_e32 v74, v74, v75
	v_cndmask_b32_e32 v76, v220, v76, vcc
	v_lshlrev_b32_e32 v225, 2, v76
	ds_bpermute_b32 v75, v225, v74
	v_xor_b32_e32 v76, 4, v220
	v_cmp_lt_i32_e32 vcc, v76, v1
	s_waitcnt lgkmcnt(0)
	v_add_f32_e32 v74, v74, v75
	v_cndmask_b32_e32 v76, v220, v76, vcc
	v_lshlrev_b32_e32 v230, 2, v76
	ds_bpermute_b32 v75, v230, v74
	v_xor_b32_e32 v76, 8, v220
	v_cmp_lt_i32_e32 vcc, v76, v1
	s_waitcnt lgkmcnt(0)
	v_add_f32_e32 v74, v74, v75
	v_cndmask_b32_e32 v76, v220, v76, vcc
	v_lshlrev_b32_e32 v231, 2, v76
	ds_bpermute_b32 v75, v231, v74
	v_xor_b32_e32 v76, 16, v220
	v_cmp_lt_i32_e32 vcc, v76, v1
	s_waitcnt lgkmcnt(0)
	v_add_f32_e32 v74, v74, v75
	v_cndmask_b32_e32 v76, v220, v76, vcc
	v_lshlrev_b32_e32 v232, 2, v76
	ds_bpermute_b32 v75, v232, v74
	v_xor_b32_e32 v76, 32, v220
	v_cmp_lt_i32_e32 vcc, v76, v1
	s_waitcnt lgkmcnt(0)
	v_add_f32_e32 v74, v74, v75
	v_cndmask_b32_e32 v1, v220, v76, vcc
	v_lshlrev_b32_e32 v1, 2, v1
	ds_bpermute_b32 v75, v1, v74
	s_waitcnt lgkmcnt(0)
	v_add_f32_e32 v70, v74, v75
	v_fmamk_f32 v70, v70, 0x3a000000, v221
	v_mul_f32_e32 v71, 0x4f800000, v70
	v_cmp_gt_f32_e32 vcc, s56, v70
	s_nop 1
	v_cndmask_b32_e32 v124, v70, v71, vcc
	v_sqrt_f32_e32 v216, v124
	global_load_dwordx4 v[94:97], v[126:127], off offset:512
	global_load_dwordx4 v[70:73], v[126:127], off offset:3072
	global_load_dwordx4 v[74:77], v[126:127], off offset:3328
	global_load_dwordx4 v[78:81], v[126:127], off offset:3584
	v_add_u32_e32 v217, -1, v216
	v_fma_f32 v226, -v217, v216, v124
	v_cmp_ge_f32_e64 s[6:7], 0, v226
	v_add_u32_e32 v226, 1, v216
	s_nop 0
	v_cndmask_b32_e64 v217, v216, v217, s[6:7]
	v_fma_f32 v216, -v226, v216, v124
	v_cmp_lt_f32_e64 s[6:7], 0, v216
	s_nop 1
	v_cndmask_b32_e64 v216, v217, v226, s[6:7]
	v_mul_f32_e32 v217, 0x37800000, v216
	v_cndmask_b32_e32 v216, v216, v217, vcc
	v_cmp_class_f32_e32 vcc, v124, v222
	s_nop 1
	v_cndmask_b32_e32 v124, v216, v124, vcc
	v_div_scale_f32 v216, s[6:7], v124, v124, 1.0
	v_rcp_f32_e32 v217, v216
	s_lshl_b64 s[6:7], s[54:55], 12
	v_fma_f32 v226, -v216, v217, 1.0
	v_fmac_f32_e32 v217, v226, v217
	v_div_scale_f32 v226, vcc, 1.0, v124, 1.0
	v_mul_f32_e32 v227, v226, v217
	v_fma_f32 v228, -v216, v227, v226
	v_fmac_f32_e32 v227, v228, v217
	v_fma_f32 v216, -v216, v227, v226
	v_div_fmas_f32 v216, v216, v217, v227
	v_div_fixup_f32 v124, v216, v124, 1.0
	v_pk_mul_f32 v[118:119], v[118:119], v[124:125] op_sel_hi:[1,0]
	v_pk_mul_f32 v[120:121], v[120:121], v[124:125] op_sel_hi:[1,0]
	v_pk_mul_f32 v[114:115], v[114:115], v[124:125] op_sel_hi:[1,0]
	v_pk_mul_f32 v[116:117], v[116:117], v[124:125] op_sel_hi:[1,0]
	v_pk_mul_f32 v[120:121], v[8:9], v[120:121]
	v_pk_mul_f32 v[118:119], v[6:7], v[118:119]
	v_pk_mul_f32 v[116:117], v[4:5], v[116:117]
	v_pk_mul_f32 v[114:115], v[2:3], v[114:115]
	v_lshl_add_u64 v[216:217], v[130:131], 0, s[6:7]
	v_cvt_pk_bf16_f32 v226, v118, v119
	v_cvt_pk_bf16_f32 v227, v120, v121
	v_cvt_pk_bf16_f32 v228, v114, v115
	v_cvt_pk_bf16_f32 v229, v116, v117
	v_pk_mul_f32 v[110:111], v[110:111], v[124:125] op_sel_hi:[1,0]
	v_pk_mul_f32 v[112:113], v[112:113], v[124:125] op_sel_hi:[1,0]
	v_pk_mul_f32 v[106:107], v[106:107], v[124:125] op_sel_hi:[1,0]
	v_pk_mul_f32 v[108:109], v[108:109], v[124:125] op_sel_hi:[1,0]
	global_store_dwordx4 v[216:217], v[226:229], off
	v_pk_mul_f32 v[112:113], v[16:17], v[112:113]
	v_pk_mul_f32 v[110:111], v[14:15], v[110:111]
	v_add_u32_e32 v226, s26, v122
	v_pk_mul_f32 v[108:109], v[12:13], v[108:109]
	v_pk_mul_f32 v[106:107], v[10:11], v[106:107]
	ds_write_b128 v226, v[118:121]
	ds_write_b128 v226, v[114:117] offset:16
	v_cvt_pk_bf16_f32 v114, v110, v111
	v_cvt_pk_bf16_f32 v115, v112, v113
	v_cvt_pk_bf16_f32 v116, v106, v107
	v_cvt_pk_bf16_f32 v117, v108, v109
	global_store_dwordx4 v[216:217], v[114:117], off offset:1024
	ds_write_b128 v226, v[110:113] offset:2048
	ds_write_b128 v226, v[106:109] offset:2064
	s_waitcnt vmcnt(15)
	v_mov_b32_e32 v108, v55
	s_waitcnt vmcnt(14)
	v_mov_b32_e32 v109, v51
	v_mov_b32_e32 v106, v54
	v_mov_b32_e32 v107, v50
	v_pk_mul_f32 v[108:109], v[108:109], v[108:109]
	v_mov_b32_e32 v110, v57
	v_mov_b32_e32 v111, v53
	v_pk_fma_f32 v[106:107], v[106:107], v[106:107], v[108:109]
	v_mov_b32_e32 v108, v56
	v_mov_b32_e32 v109, v52
	v_pk_mul_f32 v[110:111], v[110:111], v[110:111]
	v_pk_mul_f32 v[90:91], v[90:91], v[124:125] op_sel_hi:[1,0]
	v_pk_fma_f32 v[108:109], v[108:109], v[108:109], v[110:111]
	s_waitcnt vmcnt(12)
	v_pk_mul_f32 v[110:111], v[46:47], v[46:47]
	v_pk_add_f32 v[106:107], v[106:107], v[108:109]
	v_pk_mul_f32 v[108:109], v[48:49], v[48:49]
	v_pk_add_f32 v[106:107], v[106:107], v[106:107] op_sel:[0,1] op_sel_hi:[1,0]
	v_pk_mov_b32 v[112:113], v[110:111], v[108:109] op_sel:[1,0]
	v_mov_b32_e32 v111, v109
	v_pk_add_f32 v[108:109], v[112:113], v[110:111]
	s_waitcnt vmcnt(11)
	v_mul_f32_e32 v110, v38, v38
	v_mul_f32_e32 v111, v39, v39
	v_pk_add_f32 v[108:109], v[108:109], v[108:109] op_sel:[0,1] op_sel_hi:[1,0]
	v_mov_b32_e32 v107, v110
	v_mov_b32_e32 v109, v111
	v_pk_add_f32 v[106:107], v[106:107], v[108:109]
	v_mul_f32_e32 v108, v43, v43
	v_mul_f32_e32 v110, v45, v45
	v_mul_f32_e32 v112, v40, v40
	v_mul_f32_e32 v113, v41, v41
	v_pk_fma_f32 v[108:109], v[42:43], v[42:43], v[108:109] op_sel_hi:[1,1,0]
	v_pk_fma_f32 v[110:111], v[44:45], v[44:45], v[110:111] op_sel_hi:[1,1,0]
	v_mov_b32_e32 v109, v112
	v_mov_b32_e32 v111, v113
	v_pk_add_f32 v[108:109], v[108:109], v[110:111]
	s_waitcnt vmcnt(10)
	v_pk_mul_f32 v[110:111], v[34:35], v[34:35]
	v_pk_add_f32 v[106:107], v[106:107], v[108:109]
	v_pk_mul_f32 v[108:109], v[36:37], v[36:37]
	v_pk_add_f32 v[106:107], v[106:107], v[106:107] op_sel:[0,1] op_sel_hi:[1,0]
	v_pk_mov_b32 v[112:113], v[110:111], v[108:109] op_sel:[1,0]
	v_mov_b32_e32 v111, v109
	v_pk_add_f32 v[108:109], v[112:113], v[110:111]
	s_waitcnt vmcnt(8)
	v_mul_f32_e32 v110, v98, v98
	v_mul_f32_e32 v111, v99, v99
	v_pk_add_f32 v[108:109], v[108:109], v[108:109] op_sel:[0,1] op_sel_hi:[1,0]
	v_mov_b32_e32 v107, v110
	v_mov_b32_e32 v109, v111
	v_pk_add_f32 v[106:107], v[106:107], v[108:109]
	v_mul_f32_e32 v108, v103, v103
	v_mul_f32_e32 v110, v105, v105
	v_mul_f32_e32 v112, v100, v100
	v_mul_f32_e32 v113, v101, v101
	v_pk_fma_f32 v[108:109], v[102:103], v[102:103], v[108:109] op_sel_hi:[1,1,0]
	v_pk_fma_f32 v[110:111], v[104:105], v[104:105], v[110:111] op_sel_hi:[1,1,0]
	v_mov_b32_e32 v109, v112
	v_mov_b32_e32 v111, v113
	v_pk_add_f32 v[108:109], v[108:109], v[110:111]
	v_pk_mul_f32 v[92:93], v[92:93], v[124:125] op_sel_hi:[1,0]
	v_pk_add_f32 v[106:107], v[106:107], v[108:109]
	v_pk_mul_f32 v[66:67], v[66:67], v[124:125] op_sel_hi:[1,0]
	v_add_f32_e32 v106, v106, v107
	ds_bpermute_b32 v107, v218, v106
	v_pk_mul_f32 v[68:69], v[68:69], v[124:125] op_sel_hi:[1,0]
	v_pk_mul_f32 v[92:93], v[20:21], v[92:93]
	v_pk_mul_f32 v[90:91], v[18:19], v[90:91]
	v_pk_mul_f32 v[68:69], v[28:29], v[68:69]
	s_waitcnt lgkmcnt(0)
	v_add_f32_e32 v107, v106, v107
	ds_bpermute_b32 v108, v225, v107
	v_pk_mul_f32 v[66:67], v[26:27], v[66:67]
	v_cvt_pk_bf16_f32 v106, v90, v91
	v_cvt_pk_bf16_f32 v109, v68, v69
	v_pk_mul_f32 v[62:63], v[62:63], v[124:125] op_sel_hi:[1,0]
	s_waitcnt lgkmcnt(0)
	v_add_f32_e32 v110, v107, v108
	ds_bpermute_b32 v111, v230, v110
	v_cvt_pk_bf16_f32 v107, v92, v93
	v_cvt_pk_bf16_f32 v108, v66, v67
	global_store_dwordx4 v[216:217], v[106:109], off offset:2048
	ds_write_b128 v226, v[90:93] offset:4096
	ds_write_b128 v226, v[66:69] offset:4112
	s_waitcnt lgkmcnt(2)
	v_add_f32_e32 v106, v110, v111
	ds_bpermute_b32 v107, v231, v106
	v_pk_mul_f32 v[64:65], v[64:65], v[124:125] op_sel_hi:[1,0]
	v_pk_mul_f32 v[58:59], v[58:59], v[124:125] op_sel_hi:[1,0]
	v_pk_mul_f32 v[60:61], v[60:61], v[124:125] op_sel_hi:[1,0]
	v_pk_mul_f32 v[64:65], v[24:25], v[64:65]
	s_waitcnt lgkmcnt(0)
	v_add_f32_e32 v66, v106, v107
	ds_bpermute_b32 v67, v232, v66
	v_pk_mul_f32 v[62:63], v[22:23], v[62:63]
	v_pk_mul_f32 v[60:61], v[32:33], v[60:61]
	v_pk_mul_f32 v[58:59], v[30:31], v[58:59]
	v_cvt_pk_bf16_f32 v69, v60, v61
	s_waitcnt lgkmcnt(0)
	v_add_f32_e32 v68, v66, v67
	ds_bpermute_b32 v1, v1, v68
	v_cvt_pk_bf16_f32 v66, v62, v63
	v_cvt_pk_bf16_f32 v67, v64, v65
	s_waitcnt lgkmcnt(0)
	v_add_f32_e32 v1, v68, v1
	v_fmamk_f32 v1, v1, 0x3a000000, v221
	v_mul_f32_e32 v68, 0x4f800000, v1
	v_cmp_gt_f32_e32 vcc, s56, v1
	s_nop 1
	v_cndmask_b32_e32 v1, v1, v68, vcc
	v_sqrt_f32_e32 v90, v1
	v_cvt_pk_bf16_f32 v68, v58, v59
	global_store_dwordx4 v[216:217], v[66:69], off offset:3072
	ds_write_b128 v226, v[62:65] offset:6144
	ds_write_b128 v226, v[58:61] offset:6160
	v_add_u32_e32 v66, -1, v90
	v_fma_f32 v67, -v66, v90, v1
	v_cmp_ge_f32_e64 s[6:7], 0, v67
	v_add_u32_e32 v67, 1, v90
	v_fma_f32 v68, -v67, v90, v1
	v_cndmask_b32_e64 v66, v90, v66, s[6:7]
	v_cmp_lt_f32_e64 s[6:7], 0, v68
	s_nop 1
	v_cndmask_b32_e64 v66, v66, v67, s[6:7]
	v_mul_f32_e32 v67, 0x37800000, v66
	v_cndmask_b32_e32 v66, v66, v67, vcc
	v_cmp_class_f32_e32 vcc, v1, v222
	s_nop 1
	v_cndmask_b32_e32 v1, v66, v1, vcc
	v_div_scale_f32 v66, s[6:7], v1, v1, 1.0
	v_rcp_f32_e32 v67, v66
	s_lshl_b64 s[6:7], s[58:59], 12
	v_lshl_add_u64 v[64:65], v[130:131], 0, s[6:7]
	v_fma_f32 v58, -v66, v67, 1.0
	v_fmac_f32_e32 v67, v58, v67
	v_div_scale_f32 v58, vcc, 1.0, v1, 1.0
	v_mul_f32_e32 v59, v58, v67
	v_fma_f32 v60, -v66, v59, v58
	v_fmac_f32_e32 v59, v60, v67
	v_fma_f32 v58, -v66, v59, v58
	v_div_fmas_f32 v58, v58, v67, v59
	v_div_fixup_f32 v62, v58, v1, 1.0
	v_pk_mul_f32 v[54:55], v[54:55], v[62:63] op_sel_hi:[1,0]
	v_pk_mul_f32 v[56:57], v[56:57], v[62:63] op_sel_hi:[1,0]
	v_pk_mul_f32 v[50:51], v[50:51], v[62:63] op_sel_hi:[1,0]
	v_pk_mul_f32 v[52:53], v[52:53], v[62:63] op_sel_hi:[1,0]
	v_pk_mul_f32 v[56:57], v[8:9], v[56:57]
	v_pk_mul_f32 v[54:55], v[6:7], v[54:55]
	v_pk_mul_f32 v[52:53], v[4:5], v[52:53]
	v_pk_mul_f32 v[50:51], v[2:3], v[50:51]
	v_pk_mul_f32 v[46:47], v[46:47], v[62:63] op_sel_hi:[1,0]
	v_pk_mul_f32 v[48:49], v[48:49], v[62:63] op_sel_hi:[1,0]
	v_pk_mul_f32 v[42:43], v[42:43], v[62:63] op_sel_hi:[1,0]
	v_pk_mul_f32 v[44:45], v[44:45], v[62:63] op_sel_hi:[1,0]
	v_cvt_pk_bf16_f32 v58, v54, v55
	v_cvt_pk_bf16_f32 v59, v56, v57
	v_cvt_pk_bf16_f32 v60, v50, v51
	v_cvt_pk_bf16_f32 v61, v52, v53
	v_add_u32_e32 v1, s33, v122
	v_pk_mul_f32 v[48:49], v[16:17], v[48:49]
	v_pk_mul_f32 v[46:47], v[14:15], v[46:47]
	v_pk_mul_f32 v[44:45], v[12:13], v[44:45]
	v_pk_mul_f32 v[42:43], v[10:11], v[42:43]
	v_pk_mul_f32 v[38:39], v[38:39], v[62:63] op_sel_hi:[1,0]
	v_pk_mul_f32 v[40:41], v[40:41], v[62:63] op_sel_hi:[1,0]
	v_pk_mul_f32 v[34:35], v[34:35], v[62:63] op_sel_hi:[1,0]
	v_pk_mul_f32 v[36:37], v[36:37], v[62:63] op_sel_hi:[1,0]
	global_store_dwordx4 v[64:65], v[58:61], off
	ds_write_b128 v1, v[54:57]
	ds_write_b128 v1, v[50:53] offset:16
	v_cvt_pk_bf16_f32 v50, v46, v47
	v_cvt_pk_bf16_f32 v51, v48, v49
	v_cvt_pk_bf16_f32 v52, v42, v43
	v_cvt_pk_bf16_f32 v53, v44, v45
	v_pk_mul_f32 v[40:41], v[20:21], v[40:41]
	v_pk_mul_f32 v[38:39], v[18:19], v[38:39]
	v_pk_mul_f32 v[36:37], v[28:29], v[36:37]
	v_pk_mul_f32 v[34:35], v[26:27], v[34:35]
	global_store_dwordx4 v[64:65], v[50:53], off offset:1024
	ds_write_b128 v1, v[46:49] offset:2048
	ds_write_b128 v1, v[42:45] offset:2064
	v_cvt_pk_bf16_f32 v42, v38, v39
	v_cvt_pk_bf16_f32 v43, v40, v41
	v_cvt_pk_bf16_f32 v44, v34, v35
	v_cvt_pk_bf16_f32 v45, v36, v37
	global_store_dwordx4 v[64:65], v[42:45], off offset:2048
	ds_write_b128 v1, v[38:41] offset:4096
	ds_write_b128 v1, v[34:37] offset:4112
	v_pk_mul_f32 v[34:35], v[102:103], v[62:63] op_sel_hi:[1,0]
	v_pk_mul_f32 v[36:37], v[104:105], v[62:63] op_sel_hi:[1,0]
	v_pk_mul_f32 v[38:39], v[98:99], v[62:63] op_sel_hi:[1,0]
	v_pk_mul_f32 v[40:41], v[100:101], v[62:63] op_sel_hi:[1,0]
	v_pk_mul_f32 v[36:37], v[24:25], v[36:37]
	v_pk_mul_f32 v[34:35], v[22:23], v[34:35]
	v_pk_mul_f32 v[40:41], v[32:33], v[40:41]
	v_pk_mul_f32 v[38:39], v[30:31], v[38:39]
	v_cvt_pk_bf16_f32 v42, v34, v35
	v_cvt_pk_bf16_f32 v43, v36, v37
	v_cvt_pk_bf16_f32 v44, v38, v39
	v_cvt_pk_bf16_f32 v45, v40, v41
	global_store_dwordx4 v[64:65], v[42:45], off offset:3072
	ds_write_b128 v1, v[34:37] offset:6144
	ds_write_b128 v1, v[38:41] offset:6160
	s_waitcnt lgkmcnt(0)
	s_barrier
	global_load_dwordx4 v[34:37], v[132:133], off
	global_load_dwordx4 v[38:41], v[134:135], off
	global_load_dwordx4 v[42:45], v[136:137], off
	global_load_dwordx4 v[46:49], v[138:139], off
	global_load_dwordx4 v[50:53], v[140:141], off
	global_load_dwordx4 v[54:57], v[142:143], off
	global_load_dwordx4 v[58:61], v[144:145], off
	global_load_dwordx4 v[62:65], v[146:147], off
	global_load_dwordx4 v[66:69], v[148:149], off
	global_load_dwordx4 v[90:93], v[150:151], off
	global_load_dwordx4 v[98:101], v[152:153], off
	global_load_dwordx4 v[102:105], v[154:155], off
	global_load_dwordx4 v[106:109], v[156:157], off
	global_load_dwordx4 v[110:113], v[158:159], off
	global_load_dwordx4 v[114:117], v[160:161], off
	global_load_dwordx4 v[118:121], v[162:163], off
	global_load_dwordx4 v[226:229], v[164:165], off
	global_load_dwordx4 v[230:233], v[166:167], off
	ds_read_b128 v[234:237], v123
	ds_read_b128 v[238:241], v123 offset:64
	s_waitcnt vmcnt(31) lgkmcnt(1)
	v_mfma_f32_16x16x4_f32 v[242:245], v234, v82, 0
	s_waitcnt vmcnt(30)
	v_mfma_f32_16x16x4_f32 v[246:249], v234, v86, 0
	s_waitcnt vmcnt(29)
	v_mfma_f32_16x16x4_f32 v[250:253], v234, v94, 0
	v_mfma_f32_16x16x4_f32 v[242:245], v235, v83, v[242:245]
	v_mfma_f32_16x16x4_f32 v[246:249], v235, v87, v[246:249]
	v_mfma_f32_16x16x4_f32 v[250:253], v235, v95, v[250:253]
	v_mfma_f32_16x16x4_f32 v[242:245], v236, v84, v[242:245]
	v_mfma_f32_16x16x4_f32 v[246:249], v236, v88, v[246:249]
	v_mfma_f32_16x16x4_f32 v[250:253], v236, v96, v[250:253]
	v_mfma_f32_16x16x4_f32 v[82:85], v237, v85, v[242:245]
	v_mfma_f32_16x16x4_f32 v[86:89], v237, v89, v[246:249]
	v_mfma_f32_16x16x4_f32 v[94:97], v237, v97, v[250:253]
	s_waitcnt vmcnt(28) lgkmcnt(0)
	v_mfma_f32_16x16x4_f32 v[82:85], v238, v70, v[82:85]
	s_waitcnt vmcnt(27)
	v_mfma_f32_16x16x4_f32 v[86:89], v238, v74, v[86:89]
	s_waitcnt vmcnt(26)
	v_mfma_f32_16x16x4_f32 v[94:97], v238, v78, v[94:97]
	v_mfma_f32_16x16x4_f32 v[82:85], v239, v71, v[82:85]
	v_mfma_f32_16x16x4_f32 v[86:89], v239, v75, v[86:89]
	v_mfma_f32_16x16x4_f32 v[94:97], v239, v79, v[94:97]
	v_mfma_f32_16x16x4_f32 v[82:85], v240, v72, v[82:85]
	v_mfma_f32_16x16x4_f32 v[86:89], v240, v76, v[86:89]
	v_mfma_f32_16x16x4_f32 v[94:97], v240, v80, v[94:97]
	v_mfma_f32_16x16x4_f32 v[70:73], v241, v73, v[82:85]
	v_mfma_f32_16x16x4_f32 v[74:77], v241, v77, v[86:89]
	s_nop 5
	ds_read_b128 v[82:85], v123 offset:128
	ds_read_b128 v[86:89], v123 offset:192
	v_mfma_f32_16x16x4_f32 v[78:81], v241, v81, v[94:97]
	s_waitcnt vmcnt(17) lgkmcnt(1)
	v_mfma_f32_16x16x4_f32 v[70:73], v82, v34, v[70:73]
	s_waitcnt vmcnt(16)
	v_mfma_f32_16x16x4_f32 v[74:77], v82, v38, v[74:77]
	s_waitcnt vmcnt(15)
	v_mfma_f32_16x16x4_f32 v[78:81], v82, v42, v[78:81]
	v_mfma_f32_16x16x4_f32 v[70:73], v83, v35, v[70:73]
	v_mfma_f32_16x16x4_f32 v[74:77], v83, v39, v[74:77]
	v_mfma_f32_16x16x4_f32 v[78:81], v83, v43, v[78:81]
	v_mfma_f32_16x16x4_f32 v[70:73], v84, v36, v[70:73]
	v_mfma_f32_16x16x4_f32 v[74:77], v84, v40, v[74:77]
	v_mfma_f32_16x16x4_f32 v[78:81], v84, v44, v[78:81]
	v_mfma_f32_16x16x4_f32 v[34:37], v85, v37, v[70:73]
	v_mfma_f32_16x16x4_f32 v[38:41], v85, v41, v[74:77]
	v_mfma_f32_16x16x4_f32 v[42:45], v85, v45, v[78:81]
	s_waitcnt vmcnt(12) lgkmcnt(0)
	v_mfma_f32_16x16x4_f32 v[42:45], v86, v54, v[42:45]
	v_mfma_f32_16x16x4_f32 v[34:37], v86, v46, v[34:37]
	v_mfma_f32_16x16x4_f32 v[38:41], v86, v50, v[38:41]
	v_mfma_f32_16x16x4_f32 v[42:45], v87, v55, v[42:45]
	v_mfma_f32_16x16x4_f32 v[34:37], v87, v47, v[34:37]
	v_mfma_f32_16x16x4_f32 v[38:41], v87, v51, v[38:41]
	v_mfma_f32_16x16x4_f32 v[42:45], v88, v56, v[42:45]
	v_mfma_f32_16x16x4_f32 v[34:37], v88, v48, v[34:37]
	v_mfma_f32_16x16x4_f32 v[38:41], v88, v52, v[38:41]
	v_mfma_f32_16x16x4_f32 v[34:37], v89, v49, v[34:37]
	global_load_dwordx4 v[46:49], v[168:169], off
	global_load_dwordx4 v[70:73], v[170:171], off
	global_load_dwordx4 v[74:77], v[172:173], off
	global_load_dwordx4 v[78:81], v[174:175], off
	v_mfma_f32_16x16x4_f32 v[38:41], v89, v53, v[38:41]
	global_load_dwordx4 v[50:53], v[176:177], off
	global_load_dwordx4 v[82:85], v[178:179], off
	global_load_dwordx4 v[94:97], v[180:181], off
	global_load_dwordx4 v[234:237], v[182:183], off
	global_load_dwordx4 v[238:241], v[184:185], off
	global_load_dwordx4 v[242:245], v[186:187], off
	global_load_dwordx4 v[246:249], v[188:189], off
	global_load_dwordx4 v[250:253], v[190:191], off
	v_mfma_f32_16x16x4_f32 v[42:45], v89, v57, v[42:45]
	ds_read_b128 v[54:57], v123 offset:256
	ds_read_b128 v[86:89], v123 offset:320
	s_waitcnt vmcnt(23) lgkmcnt(1)
	v_mfma_f32_16x16x4_f32 v[34:37], v54, v58, v[34:37]
	s_waitcnt vmcnt(22)
	v_mfma_f32_16x16x4_f32 v[38:41], v54, v62, v[38:41]
	s_waitcnt vmcnt(21)
	v_mfma_f32_16x16x4_f32 v[42:45], v54, v66, v[42:45]
	v_mfma_f32_16x16x4_f32 v[34:37], v55, v59, v[34:37]
	v_mfma_f32_16x16x4_f32 v[38:41], v55, v63, v[38:41]
	v_mfma_f32_16x16x4_f32 v[42:45], v55, v67, v[42:45]
	v_mfma_f32_16x16x4_f32 v[34:37], v56, v60, v[34:37]
	v_mfma_f32_16x16x4_f32 v[38:41], v56, v64, v[38:41]
	v_mfma_f32_16x16x4_f32 v[42:45], v56, v68, v[42:45]
	v_mfma_f32_16x16x4_f32 v[34:37], v57, v61, v[34:37]
	v_mfma_f32_16x16x4_f32 v[38:41], v57, v65, v[38:41]
	v_mfma_f32_16x16x4_f32 v[42:45], v57, v69, v[42:45]
	ds_read_b128 v[54:57], v123 offset:384
	ds_read_b128 v[58:61], v123 offset:448
	s_waitcnt vmcnt(20) lgkmcnt(2)
	v_mfma_f32_16x16x4_f32 v[34:37], v86, v90, v[34:37]
	s_waitcnt vmcnt(19)
	v_mfma_f32_16x16x4_f32 v[38:41], v86, v98, v[38:41]
	s_waitcnt vmcnt(18)
	v_mfma_f32_16x16x4_f32 v[42:45], v86, v102, v[42:45]
	v_mfma_f32_16x16x4_f32 v[34:37], v87, v91, v[34:37]
	v_mfma_f32_16x16x4_f32 v[38:41], v87, v99, v[38:41]
	v_mfma_f32_16x16x4_f32 v[42:45], v87, v103, v[42:45]
	v_mfma_f32_16x16x4_f32 v[34:37], v88, v92, v[34:37]
	v_mfma_f32_16x16x4_f32 v[38:41], v88, v100, v[38:41]
	v_mfma_f32_16x16x4_f32 v[42:45], v88, v104, v[42:45]
	v_mfma_f32_16x16x4_f32 v[34:37], v89, v93, v[34:37]
	v_mfma_f32_16x16x4_f32 v[38:41], v89, v101, v[38:41]
	v_mfma_f32_16x16x4_f32 v[42:45], v89, v105, v[42:45]
	s_waitcnt vmcnt(17) lgkmcnt(1)
	v_mfma_f32_16x16x4_f32 v[34:37], v54, v106, v[34:37]
	s_waitcnt vmcnt(16)
	v_mfma_f32_16x16x4_f32 v[38:41], v54, v110, v[38:41]
	s_waitcnt vmcnt(15)
	v_mfma_f32_16x16x4_f32 v[42:45], v54, v114, v[42:45]
	v_mfma_f32_16x16x4_f32 v[34:37], v55, v107, v[34:37]
	v_mfma_f32_16x16x4_f32 v[38:41], v55, v111, v[38:41]
	v_mfma_f32_16x16x4_f32 v[42:45], v55, v115, v[42:45]
	v_mfma_f32_16x16x4_f32 v[34:37], v56, v108, v[34:37]
	v_mfma_f32_16x16x4_f32 v[38:41], v56, v112, v[38:41]
	v_mfma_f32_16x16x4_f32 v[42:45], v56, v116, v[42:45]
	v_mfma_f32_16x16x4_f32 v[34:37], v57, v109, v[34:37]
	v_mfma_f32_16x16x4_f32 v[38:41], v57, v113, v[38:41]
	v_mfma_f32_16x16x4_f32 v[42:45], v57, v117, v[42:45]
	global_load_dwordx4 v[54:57], v[192:193], off
	global_load_dwordx4 v[62:65], v[194:195], off
	global_load_dwordx4 v[66:69], v[196:197], off
	global_load_dwordx4 v[86:89], v[198:199], off
	s_waitcnt vmcnt(16) lgkmcnt(0)
	v_mfma_f32_16x16x4_f32 v[42:45], v58, v230, v[42:45]
	v_mfma_f32_16x16x4_f32 v[34:37], v58, v118, v[34:37]
	v_mfma_f32_16x16x4_f32 v[38:41], v58, v226, v[38:41]
	v_mfma_f32_16x16x4_f32 v[42:45], v59, v231, v[42:45]
	v_mfma_f32_16x16x4_f32 v[34:37], v59, v119, v[34:37]
	v_mfma_f32_16x16x4_f32 v[38:41], v59, v227, v[38:41]
	v_mfma_f32_16x16x4_f32 v[42:45], v60, v232, v[42:45]
	v_mfma_f32_16x16x4_f32 v[34:37], v60, v120, v[34:37]
	v_mfma_f32_16x16x4_f32 v[38:41], v60, v228, v[38:41]
	v_mfma_f32_16x16x4_f32 v[34:37], v61, v121, v[34:37]
	v_mfma_f32_16x16x4_f32 v[38:41], v61, v229, v[38:41]
	global_load_dwordx4 v[90:93], v[200:201], off
	global_load_dwordx4 v[98:101], v[202:203], off
	global_load_dwordx4 v[102:105], v[204:205], off
	global_load_dwordx4 v[106:109], v[206:207], off
	global_load_dwordx4 v[110:113], v[208:209], off
	global_load_dwordx4 v[114:117], v[210:211], off
	global_load_dwordx4 v[118:121], v[212:213], off
	global_load_dwordx4 v[226:229], v[214:215], off
	v_mfma_f32_16x16x4_f32 v[42:45], v61, v233, v[42:45]
	ds_read_b128 v[58:61], v123 offset:512
	ds_read_b128 v[230:233], v123 offset:576
	s_waitcnt vmcnt(23) lgkmcnt(1)
	v_mfma_f32_16x16x4_f32 v[34:37], v58, v46, v[34:37]
	s_waitcnt vmcnt(22)
	v_mfma_f32_16x16x4_f32 v[38:41], v58, v70, v[38:41]
	s_waitcnt vmcnt(21)
	v_mfma_f32_16x16x4_f32 v[42:45], v58, v74, v[42:45]
	v_mfma_f32_16x16x4_f32 v[34:37], v59, v47, v[34:37]
	v_mfma_f32_16x16x4_f32 v[38:41], v59, v71, v[38:41]
	v_mfma_f32_16x16x4_f32 v[42:45], v59, v75, v[42:45]
	v_mfma_f32_16x16x4_f32 v[34:37], v60, v48, v[34:37]
	v_mfma_f32_16x16x4_f32 v[38:41], v60, v72, v[38:41]
	v_mfma_f32_16x16x4_f32 v[42:45], v60, v76, v[42:45]
	v_mfma_f32_16x16x4_f32 v[34:37], v61, v49, v[34:37]
	v_mfma_f32_16x16x4_f32 v[38:41], v61, v73, v[38:41]
	v_mfma_f32_16x16x4_f32 v[42:45], v61, v77, v[42:45]
	s_waitcnt vmcnt(20) lgkmcnt(0)
	v_mfma_f32_16x16x4_f32 v[34:37], v230, v78, v[34:37]
	s_waitcnt vmcnt(19)
	v_mfma_f32_16x16x4_f32 v[38:41], v230, v50, v[38:41]
	s_waitcnt vmcnt(18)
	v_mfma_f32_16x16x4_f32 v[42:45], v230, v82, v[42:45]
	v_mfma_f32_16x16x4_f32 v[34:37], v231, v79, v[34:37]
	v_mfma_f32_16x16x4_f32 v[38:41], v231, v51, v[38:41]
	v_mfma_f32_16x16x4_f32 v[42:45], v231, v83, v[42:45]
	v_mfma_f32_16x16x4_f32 v[34:37], v232, v80, v[34:37]
	v_mfma_f32_16x16x4_f32 v[38:41], v232, v52, v[38:41]
	v_mfma_f32_16x16x4_f32 v[42:45], v232, v84, v[42:45]
	v_mfma_f32_16x16x4_f32 v[34:37], v233, v81, v[34:37]
	v_mfma_f32_16x16x4_f32 v[38:41], v233, v53, v[38:41]
	ds_read_b128 v[46:49], v123 offset:640
	ds_read_b128 v[50:53], v123 offset:704
	v_mfma_f32_16x16x4_f32 v[42:45], v233, v85, v[42:45]
	s_waitcnt vmcnt(17) lgkmcnt(1)
	v_mfma_f32_16x16x4_f32 v[34:37], v46, v94, v[34:37]
	s_waitcnt vmcnt(16)
	v_mfma_f32_16x16x4_f32 v[38:41], v46, v234, v[38:41]
	s_waitcnt vmcnt(15)
	v_mfma_f32_16x16x4_f32 v[42:45], v46, v238, v[42:45]
	v_mfma_f32_16x16x4_f32 v[34:37], v47, v95, v[34:37]
	v_mfma_f32_16x16x4_f32 v[38:41], v47, v235, v[38:41]
	v_mfma_f32_16x16x4_f32 v[42:45], v47, v239, v[42:45]
	v_mfma_f32_16x16x4_f32 v[34:37], v48, v96, v[34:37]
	v_mfma_f32_16x16x4_f32 v[38:41], v48, v236, v[38:41]
	v_mfma_f32_16x16x4_f32 v[42:45], v48, v240, v[42:45]
	v_mfma_f32_16x16x4_f32 v[34:37], v49, v97, v[34:37]
	v_mfma_f32_16x16x4_f32 v[38:41], v49, v237, v[38:41]
	v_mfma_f32_16x16x4_f32 v[42:45], v49, v241, v[42:45]
	s_waitcnt vmcnt(14) lgkmcnt(0)
	v_mfma_f32_16x16x4_f32 v[34:37], v50, v242, v[34:37]
	s_waitcnt vmcnt(13)
	v_mfma_f32_16x16x4_f32 v[38:41], v50, v246, v[38:41]
	s_waitcnt vmcnt(12)
	v_mfma_f32_16x16x4_f32 v[42:45], v50, v250, v[42:45]
	v_mfma_f32_16x16x4_f32 v[34:37], v51, v243, v[34:37]
	v_mfma_f32_16x16x4_f32 v[38:41], v51, v247, v[38:41]
	v_mfma_f32_16x16x4_f32 v[42:45], v51, v251, v[42:45]
	v_mfma_f32_16x16x4_f32 v[34:37], v52, v244, v[34:37]
	v_mfma_f32_16x16x4_f32 v[38:41], v52, v248, v[38:41]
	v_mfma_f32_16x16x4_f32 v[42:45], v52, v252, v[42:45]
	v_mfma_f32_16x16x4_f32 v[34:37], v53, v245, v[34:37]
	v_mfma_f32_16x16x4_f32 v[38:41], v53, v249, v[38:41]
	v_mfma_f32_16x16x4_f32 v[42:45], v53, v253, v[42:45]
	ds_read_b128 v[46:49], v123 offset:768
	ds_read_b128 v[50:53], v123 offset:832
	s_waitcnt vmcnt(11) lgkmcnt(1)
	v_mfma_f32_16x16x4_f32 v[34:37], v46, v54, v[34:37]
	s_waitcnt vmcnt(10)
	v_mfma_f32_16x16x4_f32 v[38:41], v46, v62, v[38:41]
	s_waitcnt vmcnt(9)
	v_mfma_f32_16x16x4_f32 v[42:45], v46, v66, v[42:45]
	v_mfma_f32_16x16x4_f32 v[34:37], v47, v55, v[34:37]
	v_mfma_f32_16x16x4_f32 v[38:41], v47, v63, v[38:41]
	v_mfma_f32_16x16x4_f32 v[42:45], v47, v67, v[42:45]
	v_mfma_f32_16x16x4_f32 v[34:37], v48, v56, v[34:37]
	v_mfma_f32_16x16x4_f32 v[38:41], v48, v64, v[38:41]
	v_mfma_f32_16x16x4_f32 v[42:45], v48, v68, v[42:45]
	v_mfma_f32_16x16x4_f32 v[34:37], v49, v57, v[34:37]
	v_mfma_f32_16x16x4_f32 v[38:41], v49, v65, v[38:41]
	v_mfma_f32_16x16x4_f32 v[42:45], v49, v69, v[42:45]
	s_waitcnt vmcnt(8) lgkmcnt(0)
	v_mfma_f32_16x16x4_f32 v[34:37], v50, v86, v[34:37]
	s_waitcnt vmcnt(7)
	v_mfma_f32_16x16x4_f32 v[38:41], v50, v90, v[38:41]
	s_waitcnt vmcnt(6)
	v_mfma_f32_16x16x4_f32 v[42:45], v50, v98, v[42:45]
	v_mfma_f32_16x16x4_f32 v[34:37], v51, v87, v[34:37]
	v_mfma_f32_16x16x4_f32 v[38:41], v51, v91, v[38:41]
	v_mfma_f32_16x16x4_f32 v[42:45], v51, v99, v[42:45]
	v_mfma_f32_16x16x4_f32 v[34:37], v52, v88, v[34:37]
	v_mfma_f32_16x16x4_f32 v[38:41], v52, v92, v[38:41]
	v_mfma_f32_16x16x4_f32 v[42:45], v52, v100, v[42:45]
	v_mfma_f32_16x16x4_f32 v[34:37], v53, v89, v[34:37]
	v_mfma_f32_16x16x4_f32 v[38:41], v53, v93, v[38:41]
	v_mfma_f32_16x16x4_f32 v[42:45], v53, v101, v[42:45]
	ds_read_b128 v[46:49], v123 offset:896
	ds_read_b128 v[50:53], v123 offset:960
	s_waitcnt vmcnt(5) lgkmcnt(1)
	v_mfma_f32_16x16x4_f32 v[34:37], v46, v102, v[34:37]
	s_waitcnt vmcnt(4)
	v_mfma_f32_16x16x4_f32 v[38:41], v46, v106, v[38:41]
	s_waitcnt vmcnt(3)
	v_mfma_f32_16x16x4_f32 v[42:45], v46, v110, v[42:45]
	v_mfma_f32_16x16x4_f32 v[34:37], v47, v103, v[34:37]
	v_mfma_f32_16x16x4_f32 v[38:41], v47, v107, v[38:41]
	v_mfma_f32_16x16x4_f32 v[42:45], v47, v111, v[42:45]
	v_mfma_f32_16x16x4_f32 v[34:37], v48, v104, v[34:37]
	v_mfma_f32_16x16x4_f32 v[38:41], v48, v108, v[38:41]
	v_mfma_f32_16x16x4_f32 v[42:45], v48, v112, v[42:45]
	v_mfma_f32_16x16x4_f32 v[34:37], v49, v105, v[34:37]
	v_mfma_f32_16x16x4_f32 v[38:41], v49, v109, v[38:41]
	v_mfma_f32_16x16x4_f32 v[42:45], v49, v113, v[42:45]
	s_waitcnt vmcnt(2) lgkmcnt(0)
	v_mfma_f32_16x16x4_f32 v[34:37], v50, v114, v[34:37]
	s_waitcnt vmcnt(1)
	v_mfma_f32_16x16x4_f32 v[38:41], v50, v118, v[38:41]
	s_waitcnt vmcnt(0)
	v_mfma_f32_16x16x4_f32 v[42:45], v50, v226, v[42:45]
	v_mfma_f32_16x16x4_f32 v[34:37], v51, v115, v[34:37]
	v_mfma_f32_16x16x4_f32 v[38:41], v51, v119, v[38:41]
	v_mfma_f32_16x16x4_f32 v[42:45], v51, v227, v[42:45]
	v_mfma_f32_16x16x4_f32 v[34:37], v52, v116, v[34:37]
	v_mfma_f32_16x16x4_f32 v[38:41], v52, v120, v[38:41]
	v_mfma_f32_16x16x4_f32 v[42:45], v52, v228, v[42:45]
	v_mfma_f32_16x16x4_f32 v[34:37], v53, v117, v[34:37]
	v_mfma_f32_16x16x4_f32 v[38:41], v53, v121, v[38:41]
	v_mfma_f32_16x16x4_f32 v[42:45], v53, v229, v[42:45]
	s_cmp_gt_u32 s68, 2
	s_cbranch_scc1 .Lrpf_a_skip
	s_add_i32 s82, s68, 1
	s_lshl_b32 s82, s82, 4
	s_add_i32 s82, s67, s82
	s_ashr_i32 s83, s82, 31
	s_lshl_b64 s[82:83], s[82:83], 13
	v_lshl_add_u64 v[98:99], v[128:129], 0, s[82:83]
	s_add_u32 s82, s82, 0x1000
	s_addc_u32 s83, s83, 0
	global_load_dwordx4 v[118:121], v[98:99], off
	global_load_dwordx4 v[114:117], v[98:99], off offset:16
	global_load_dwordx4 v[110:113], v[98:99], off offset:2048
	global_load_dwordx4 v[106:109], v[98:99], off offset:2064
	v_lshl_add_u64 v[100:101], v[128:129], 0, s[82:83]
	s_add_u32 s82, s82, 0x1000
	s_addc_u32 s83, s83, 0
	global_load_dwordx4 v[58:61], v[100:101], off offset:2064
	global_load_dwordx4 v[90:93], v[100:101], off
	global_load_dwordx4 v[66:69], v[100:101], off offset:16
	global_load_dwordx4 v[62:65], v[100:101], off offset:2048
	v_lshl_add_u64 v[98:99], v[128:129], 0, s[82:83]
	s_nop 0
	global_load_dwordx4 v[54:57], v[98:99], off
	global_load_dwordx4 v[50:53], v[98:99], off offset:16
	global_load_dwordx4 v[234:237], v[98:99], off offset:2064
	global_load_dwordx4 v[238:241], v[98:99], off offset:2048
	s_add_u32 s82, s82, 0x1000
	s_addc_u32 s83, s83, 0
	v_lshl_add_u64 v[100:101], v[128:129], 0, s[82:83]
	s_nop 0
	global_load_dwordx4 v[242:245], v[100:101], off
	global_load_dwordx4 v[246:249], v[100:101], off offset:16
	global_load_dwordx4 v[102:105], v[100:101], off offset:2048
	global_load_dwordx4 v[250:253], v[100:101], off offset:2064

.LBB0_1298:
	s_and_saveexec_b64 s[6:7], s[10:11]
	ds_write_b32 v218, v125
	s_or_b64 exec, exec, s[6:7]
	s_lshl_b32 s75, s93, 6
	s_add_i32 s76, s75, s2
	s_mov_b32 s77, 0
	s_waitcnt lgkmcnt(0)
	s_barrier
	s_mov_b32 s82, 0
	s_lshl_b32 s82, s82, 4
	s_add_i32 s82, s76, s82
	s_ashr_i32 s83, s82, 31
	s_lshl_b64 s[82:83], s[82:83], 13
	v_lshl_add_u64 v[98:99], v[128:129], 0, s[82:83]
	s_add_u32 s82, s82, 0x1000
	s_addc_u32 s83, s83, 0
	global_load_dwordx4 v[118:121], v[98:99], off
	global_load_dwordx4 v[114:117], v[98:99], off offset:16
	global_load_dwordx4 v[110:113], v[98:99], off offset:2048
	global_load_dwordx4 v[106:109], v[98:99], off offset:2064
	v_lshl_add_u64 v[100:101], v[128:129], 0, s[82:83]
	s_add_u32 s82, s82, 0x1000
	s_addc_u32 s83, s83, 0
	global_load_dwordx4 v[58:61], v[100:101], off offset:2064
	global_load_dwordx4 v[90:93], v[100:101], off
	global_load_dwordx4 v[66:69], v[100:101], off offset:16
	global_load_dwordx4 v[62:65], v[100:101], off offset:2048
	v_lshl_add_u64 v[98:99], v[128:129], 0, s[82:83]
	s_nop 0
	global_load_dwordx4 v[54:57], v[98:99], off
	global_load_dwordx4 v[50:53], v[98:99], off offset:16
	global_load_dwordx4 v[234:237], v[98:99], off offset:2064
	global_load_dwordx4 v[238:241], v[98:99], off offset:2048
	s_add_u32 s82, s82, 0x1000
	s_addc_u32 s83, s83, 0
	v_lshl_add_u64 v[100:101], v[128:129], 0, s[82:83]
	s_nop 0
	global_load_dwordx4 v[242:245], v[100:101], off
	global_load_dwordx4 v[246:249], v[100:101], off offset:16
	global_load_dwordx4 v[102:105], v[100:101], off offset:2048
	global_load_dwordx4 v[250:253], v[100:101], off offset:2064
	s_branch .LBB0_1303

.LBB0_1303:
	s_lshl_b32 s8, s77, 4
	s_add_i32 s6, s76, s8
	s_ashr_i32 s7, s6, 31
	s_lshl_b64 s[12:13], s[6:7], 13
	v_lshl_add_u64 v[34:35], v[128:129], 0, s[12:13]
	v_lshl_add_u64 v[36:37], v[34:35], 0, s[56:57]
	v_add_co_u32_e32 v36, vcc, 0x1000, v34
	v_and_b32_e32 v1, 64, v220
	s_nop 0
	v_addc_co_u32_e32 v37, vcc, 0, v35, vcc
	v_lshl_add_u64 v[34:35], v[34:35], 0, s[54:55]
	v_xor_b32_e32 v34, 1, v220
	v_add_u32_e32 v1, 64, v1
	s_or_b32 s6, s6, 1
	v_cmp_lt_i32_e32 vcc, v34, v1
	s_ashr_i32 s7, s6, 31
	s_lshl_b64 s[6:7], s[6:7], 13
	v_cndmask_b32_e32 v34, v220, v34, vcc
	v_lshlrev_b32_e32 v225, 2, v34
	v_lshl_add_u64 v[34:35], v[128:129], 0, s[6:7]
	v_add_co_u32_e32 v70, vcc, s70, v34
	v_lshl_add_u64 v[36:37], v[34:35], 0, s[54:55]
	s_nop 0
	v_addc_co_u32_e32 v71, vcc, 0, v35, vcc
	v_lshl_add_u64 v[72:73], v[34:35], 0, s[56:57]
	s_nop 0
	s_add_i32 s8, s8, s75
	s_add_i32 s60, s8, s2
	s_ashr_i32 s61, s60, 31
	s_add_i32 s62, s8, s33
	s_ashr_i32 s63, s62, 31
	s_waitcnt vmcnt(13)
	v_mov_b32_e32 v76, v119
	s_waitcnt vmcnt(12)
	v_mov_b32_e32 v77, v115
	v_mov_b32_e32 v80, v121
	v_mov_b32_e32 v81, v117
	v_mov_b32_e32 v74, v118
	v_mov_b32_e32 v75, v114
	v_mov_b32_e32 v78, v120
	v_mov_b32_e32 v79, v116
	s_waitcnt vmcnt(11)
	v_pk_mul_f32 v[82:83], v[112:113], v[112:113]
	v_pk_mul_f32 v[84:85], v[110:111], v[110:111]
	v_pk_mul_f32 v[76:77], v[76:77], v[76:77]
	v_pk_mul_f32 v[80:81], v[80:81], v[80:81]
	v_pk_mov_b32 v[94:95], v[84:85], v[82:83] op_sel:[1,0]
	v_mov_b32_e32 v85, v83
	v_pk_fma_f32 v[74:75], v[74:75], v[74:75], v[76:77]
	v_pk_fma_f32 v[76:77], v[78:79], v[78:79], v[80:81]
	s_waitcnt vmcnt(10)
	v_mul_f32_e32 v86, v107, v107
	v_mul_f32_e32 v88, v109, v109
	v_pk_add_f32 v[78:79], v[94:95], v[84:85]
	v_pk_add_f32 v[74:75], v[74:75], v[76:77]
	v_pk_fma_f32 v[82:83], v[106:107], v[106:107], v[86:87] op_sel_hi:[1,1,0]
	v_pk_fma_f32 v[86:87], v[108:109], v[108:109], v[88:89] op_sel_hi:[1,1,0]
	s_waitcnt vmcnt(8)
	v_mul_f32_e32 v95, v90, v90
	v_mul_f32_e32 v100, v91, v91
	v_pk_add_f32 v[76:77], v[78:79], v[78:79] op_sel:[0,1] op_sel_hi:[1,0]
	v_pk_add_f32 v[74:75], v[74:75], v[74:75] op_sel:[0,1] op_sel_hi:[1,0]
	v_mul_f32_e32 v83, v92, v92
	v_mul_f32_e32 v87, v93, v93
	s_waitcnt vmcnt(7)
	v_pk_mul_f32 v[80:81], v[68:69], v[68:69]
	v_pk_mul_f32 v[84:85], v[66:67], v[66:67]
	v_mov_b32_e32 v77, v100
	v_mov_b32_e32 v75, v95
	v_pk_mov_b32 v[78:79], v[84:85], v[80:81] op_sel:[1,0]
	v_mov_b32_e32 v85, v81
	v_pk_add_f32 v[82:83], v[82:83], v[86:87]
	v_pk_add_f32 v[74:75], v[74:75], v[76:77]
	s_waitcnt vmcnt(6)
	v_mul_f32_e32 v88, v63, v63
	v_mul_f32_e32 v94, v65, v65
	v_pk_add_f32 v[78:79], v[78:79], v[84:85]
	v_pk_add_f32 v[74:75], v[74:75], v[82:83]
	v_mul_f32_e32 v96, v58, v58
	v_mul_f32_e32 v97, v59, v59
	v_mul_f32_e32 v98, v60, v60
	v_mul_f32_e32 v99, v61, v61
	v_pk_fma_f32 v[80:81], v[62:63], v[62:63], v[88:89] op_sel_hi:[1,1,0]
	v_pk_fma_f32 v[88:89], v[64:65], v[64:65], v[94:95] op_sel_hi:[1,1,0]
	v_pk_add_f32 v[78:79], v[78:79], v[78:79] op_sel:[0,1] op_sel_hi:[1,0]
	v_pk_add_f32 v[74:75], v[74:75], v[74:75] op_sel:[0,1] op_sel_hi:[1,0]
	v_mov_b32_e32 v81, v98
	v_mov_b32_e32 v79, v97
	v_mov_b32_e32 v75, v96
	v_mov_b32_e32 v89, v99
	v_pk_add_f32 v[74:75], v[74:75], v[78:79]
	v_pk_add_f32 v[76:77], v[80:81], v[88:89]
	s_waitcnt vmcnt(0)
	v_mov_b32_e32 v42, v234
	v_mov_b32_e32 v43, v235
	v_mov_b32_e32 v44, v236
	v_mov_b32_e32 v45, v237
	v_mov_b32_e32 v46, v238
	v_mov_b32_e32 v47, v239
	v_mov_b32_e32 v48, v240
	v_mov_b32_e32 v49, v241
	v_mov_b32_e32 v38, v242
	v_mov_b32_e32 v39, v243
	v_mov_b32_e32 v40, v244
	v_mov_b32_e32 v41, v245
	v_mov_b32_e32 v34, v246
	v_mov_b32_e32 v35, v247
	v_mov_b32_e32 v36, v248
	v_mov_b32_e32 v37, v249
	v_mov_b32_e32 v98, v250
	v_mov_b32_e32 v99, v251
	v_mov_b32_e32 v100, v252
	v_mov_b32_e32 v101, v253
	global_load_dwordx4 v[82:85], v[126:127], off
	global_load_dwordx4 v[86:89], v[126:127], off offset:256
	v_pk_add_f32 v[74:75], v[74:75], v[76:77]
	v_xor_b32_e32 v76, 2, v220
	v_add_f32_e32 v74, v74, v75
	ds_bpermute_b32 v75, v225, v74
	v_cmp_lt_i32_e32 vcc, v76, v1
	s_waitcnt lgkmcnt(0)
	v_add_f32_e32 v74, v74, v75
	v_cndmask_b32_e32 v76, v220, v76, vcc
	v_lshlrev_b32_e32 v230, 2, v76
	ds_bpermute_b32 v75, v230, v74
	v_xor_b32_e32 v76, 4, v220
	v_cmp_lt_i32_e32 vcc, v76, v1
	s_waitcnt lgkmcnt(0)
	v_add_f32_e32 v74, v74, v75
	v_cndmask_b32_e32 v76, v220, v76, vcc
	v_lshlrev_b32_e32 v231, 2, v76
	ds_bpermute_b32 v75, v231, v74
	v_xor_b32_e32 v76, 8, v220
	v_cmp_lt_i32_e32 vcc, v76, v1
	s_waitcnt lgkmcnt(0)
	v_add_f32_e32 v74, v74, v75
	v_cndmask_b32_e32 v76, v220, v76, vcc
	v_lshlrev_b32_e32 v232, 2, v76
	ds_bpermute_b32 v75, v232, v74
	v_xor_b32_e32 v76, 16, v220
	v_cmp_lt_i32_e32 vcc, v76, v1
	s_waitcnt lgkmcnt(0)
	v_add_f32_e32 v74, v74, v75
	v_cndmask_b32_e32 v76, v220, v76, vcc
	v_lshlrev_b32_e32 v233, 2, v76
	ds_bpermute_b32 v75, v233, v74
	v_xor_b32_e32 v76, 32, v220
	v_cmp_lt_i32_e32 vcc, v76, v1
	s_waitcnt lgkmcnt(0)
	v_add_f32_e32 v74, v74, v75
	v_cndmask_b32_e32 v1, v220, v76, vcc
	v_lshlrev_b32_e32 v1, 2, v1
	ds_bpermute_b32 v75, v1, v74
	s_waitcnt lgkmcnt(0)
	v_add_f32_e32 v70, v74, v75
	v_fmamk_f32 v70, v70, 0x3a000000, v221
	v_mul_f32_e32 v71, 0x4f800000, v70
	v_cmp_gt_f32_e32 vcc, s71, v70
	s_nop 1
	v_cndmask_b32_e32 v124, v70, v71, vcc
	v_sqrt_f32_e32 v216, v124
	global_load_dwordx4 v[94:97], v[126:127], off offset:512
	global_load_dwordx4 v[70:73], v[126:127], off offset:3072
	global_load_dwordx4 v[74:77], v[126:127], off offset:3328
	global_load_dwordx4 v[78:81], v[126:127], off offset:3584
	v_add_u32_e32 v217, -1, v216
	v_fma_f32 v226, -v217, v216, v124
	v_cmp_ge_f32_e64 s[6:7], 0, v226
	v_add_u32_e32 v226, 1, v216
	s_nop 0
	v_cndmask_b32_e64 v217, v216, v217, s[6:7]
	v_fma_f32 v216, -v226, v216, v124
	v_cmp_lt_f32_e64 s[6:7], 0, v216
	s_nop 1
	v_cndmask_b32_e64 v216, v217, v226, s[6:7]
	v_mul_f32_e32 v217, 0x37800000, v216
	v_cndmask_b32_e32 v216, v216, v217, vcc
	v_cmp_class_f32_e32 vcc, v124, v222
	s_nop 1
	v_cndmask_b32_e32 v124, v216, v124, vcc
	v_div_scale_f32 v216, s[6:7], v124, v124, 1.0
	v_rcp_f32_e32 v217, v216
	s_lshl_b64 s[6:7], s[60:61], 12
	v_fma_f32 v226, -v216, v217, 1.0
	v_fmac_f32_e32 v217, v226, v217
	v_div_scale_f32 v226, vcc, 1.0, v124, 1.0
	v_mul_f32_e32 v227, v226, v217
	v_fma_f32 v228, -v216, v227, v226
	v_fmac_f32_e32 v227, v228, v217
	v_fma_f32 v216, -v216, v227, v226
	v_div_fmas_f32 v216, v216, v217, v227
	v_div_fixup_f32 v124, v216, v124, 1.0
	v_pk_mul_f32 v[118:119], v[118:119], v[124:125] op_sel_hi:[1,0]
	v_pk_mul_f32 v[120:121], v[120:121], v[124:125] op_sel_hi:[1,0]
	v_pk_mul_f32 v[114:115], v[114:115], v[124:125] op_sel_hi:[1,0]
	v_pk_mul_f32 v[116:117], v[116:117], v[124:125] op_sel_hi:[1,0]
	v_pk_mul_f32 v[120:121], v[28:29], v[120:121]
	v_pk_mul_f32 v[118:119], v[26:27], v[118:119]
	v_pk_mul_f32 v[116:117], v[4:5], v[116:117]
	v_pk_mul_f32 v[114:115], v[2:3], v[114:115]
	v_lshl_add_u64 v[216:217], v[130:131], 0, s[6:7]
	v_cvt_pk_bf16_f32 v226, v118, v119
	v_cvt_pk_bf16_f32 v227, v120, v121
	v_cvt_pk_bf16_f32 v228, v114, v115
	v_cvt_pk_bf16_f32 v229, v116, v117
	v_pk_mul_f32 v[110:111], v[110:111], v[124:125] op_sel_hi:[1,0]
	v_pk_mul_f32 v[112:113], v[112:113], v[124:125] op_sel_hi:[1,0]
	v_pk_mul_f32 v[106:107], v[106:107], v[124:125] op_sel_hi:[1,0]
	v_pk_mul_f32 v[108:109], v[108:109], v[124:125] op_sel_hi:[1,0]
	global_store_dwordx4 v[216:217], v[226:229], off
	v_pk_mul_f32 v[112:113], v[8:9], v[112:113]
	v_pk_mul_f32 v[110:111], v[6:7], v[110:111]
	v_add_u32_e32 v226, s26, v122
	v_pk_mul_f32 v[108:109], v[12:13], v[108:109]
	v_pk_mul_f32 v[106:107], v[10:11], v[106:107]
	ds_write_b128 v226, v[118:121]
	ds_write_b128 v226, v[114:117] offset:16
	v_cvt_pk_bf16_f32 v114, v110, v111
	v_cvt_pk_bf16_f32 v115, v112, v113
	v_cvt_pk_bf16_f32 v116, v106, v107
	v_cvt_pk_bf16_f32 v117, v108, v109
	global_store_dwordx4 v[216:217], v[114:117], off offset:1024
	ds_write_b128 v226, v[110:113] offset:2048
	ds_write_b128 v226, v[106:109] offset:2064
	s_waitcnt vmcnt(15)
	v_mov_b32_e32 v108, v55
	s_waitcnt vmcnt(14)
	v_mov_b32_e32 v109, v51
	v_mov_b32_e32 v106, v54
	v_mov_b32_e32 v107, v50
	v_pk_mul_f32 v[108:109], v[108:109], v[108:109]
	v_mov_b32_e32 v110, v57
	v_mov_b32_e32 v111, v53
	v_pk_fma_f32 v[106:107], v[106:107], v[106:107], v[108:109]
	v_mov_b32_e32 v108, v56
	v_mov_b32_e32 v109, v52
	v_pk_mul_f32 v[110:111], v[110:111], v[110:111]
	v_pk_mul_f32 v[90:91], v[90:91], v[124:125] op_sel_hi:[1,0]
	v_pk_fma_f32 v[108:109], v[108:109], v[108:109], v[110:111]
	s_waitcnt vmcnt(12)
	v_pk_mul_f32 v[110:111], v[46:47], v[46:47]
	v_pk_add_f32 v[106:107], v[106:107], v[108:109]
	v_pk_mul_f32 v[108:109], v[48:49], v[48:49]
	v_pk_add_f32 v[106:107], v[106:107], v[106:107] op_sel:[0,1] op_sel_hi:[1,0]
	v_pk_mov_b32 v[112:113], v[110:111], v[108:109] op_sel:[1,0]
	v_mov_b32_e32 v111, v109
	v_pk_add_f32 v[108:109], v[112:113], v[110:111]
	s_waitcnt vmcnt(11)
	v_mul_f32_e32 v110, v38, v38
	v_mul_f32_e32 v111, v39, v39
	v_pk_add_f32 v[108:109], v[108:109], v[108:109] op_sel:[0,1] op_sel_hi:[1,0]
	v_mov_b32_e32 v107, v110
	v_mov_b32_e32 v109, v111
	v_pk_add_f32 v[106:107], v[106:107], v[108:109]
	v_mul_f32_e32 v108, v43, v43
	v_mul_f32_e32 v110, v45, v45
	v_mul_f32_e32 v112, v40, v40
	v_mul_f32_e32 v113, v41, v41
	v_pk_fma_f32 v[108:109], v[42:43], v[42:43], v[108:109] op_sel_hi:[1,1,0]
	v_pk_fma_f32 v[110:111], v[44:45], v[44:45], v[110:111] op_sel_hi:[1,1,0]
	v_mov_b32_e32 v109, v112
	v_mov_b32_e32 v111, v113
	v_pk_add_f32 v[108:109], v[108:109], v[110:111]
	s_waitcnt vmcnt(10)
	v_pk_mul_f32 v[110:111], v[34:35], v[34:35]
	v_pk_add_f32 v[106:107], v[106:107], v[108:109]
	v_pk_mul_f32 v[108:109], v[36:37], v[36:37]
	v_pk_add_f32 v[106:107], v[106:107], v[106:107] op_sel:[0,1] op_sel_hi:[1,0]
	v_pk_mov_b32 v[112:113], v[110:111], v[108:109] op_sel:[1,0]
	v_mov_b32_e32 v111, v109
	v_pk_add_f32 v[108:109], v[112:113], v[110:111]
	s_waitcnt vmcnt(8)
	v_mul_f32_e32 v110, v98, v98
	v_mul_f32_e32 v111, v99, v99
	v_pk_add_f32 v[108:109], v[108:109], v[108:109] op_sel:[0,1] op_sel_hi:[1,0]
	v_mov_b32_e32 v107, v110
	v_mov_b32_e32 v109, v111
	v_pk_add_f32 v[106:107], v[106:107], v[108:109]
	v_mul_f32_e32 v108, v103, v103
	v_mul_f32_e32 v110, v105, v105
	v_mul_f32_e32 v112, v100, v100
	v_mul_f32_e32 v113, v101, v101
	v_pk_fma_f32 v[108:109], v[102:103], v[102:103], v[108:109] op_sel_hi:[1,1,0]
	v_pk_fma_f32 v[110:111], v[104:105], v[104:105], v[110:111] op_sel_hi:[1,1,0]
	v_mov_b32_e32 v109, v112
	v_mov_b32_e32 v111, v113
	v_pk_add_f32 v[108:109], v[108:109], v[110:111]
	v_pk_mul_f32 v[92:93], v[92:93], v[124:125] op_sel_hi:[1,0]
	v_pk_add_f32 v[106:107], v[106:107], v[108:109]
	v_pk_mul_f32 v[66:67], v[66:67], v[124:125] op_sel_hi:[1,0]
	v_add_f32_e32 v106, v106, v107
	ds_bpermute_b32 v107, v225, v106
	v_pk_mul_f32 v[68:69], v[68:69], v[124:125] op_sel_hi:[1,0]
	v_pk_mul_f32 v[92:93], v[20:21], v[92:93]
	v_pk_mul_f32 v[90:91], v[18:19], v[90:91]
	v_pk_mul_f32 v[68:69], v[16:17], v[68:69]
	s_waitcnt lgkmcnt(0)
	v_add_f32_e32 v107, v106, v107
	ds_bpermute_b32 v108, v230, v107
	v_pk_mul_f32 v[66:67], v[14:15], v[66:67]
	v_cvt_pk_bf16_f32 v106, v90, v91
	v_cvt_pk_bf16_f32 v109, v68, v69
	v_pk_mul_f32 v[62:63], v[62:63], v[124:125] op_sel_hi:[1,0]
	s_waitcnt lgkmcnt(0)
	v_add_f32_e32 v110, v107, v108
	ds_bpermute_b32 v111, v231, v110
	v_cvt_pk_bf16_f32 v107, v92, v93
	v_cvt_pk_bf16_f32 v108, v66, v67
	global_store_dwordx4 v[216:217], v[106:109], off offset:2048
	ds_write_b128 v226, v[90:93] offset:4096
	ds_write_b128 v226, v[66:69] offset:4112
	s_waitcnt lgkmcnt(2)
	v_add_f32_e32 v106, v110, v111
	ds_bpermute_b32 v107, v232, v106
	v_pk_mul_f32 v[64:65], v[64:65], v[124:125] op_sel_hi:[1,0]
	v_pk_mul_f32 v[58:59], v[58:59], v[124:125] op_sel_hi:[1,0]
	v_pk_mul_f32 v[60:61], v[60:61], v[124:125] op_sel_hi:[1,0]
	v_pk_mul_f32 v[64:65], v[24:25], v[64:65]
	s_waitcnt lgkmcnt(0)
	v_add_f32_e32 v66, v106, v107
	ds_bpermute_b32 v67, v233, v66
	v_pk_mul_f32 v[62:63], v[22:23], v[62:63]
	v_pk_mul_f32 v[60:61], v[32:33], v[60:61]
	v_pk_mul_f32 v[58:59], v[30:31], v[58:59]
	v_cvt_pk_bf16_f32 v69, v60, v61
	s_waitcnt lgkmcnt(0)
	v_add_f32_e32 v68, v66, v67
	ds_bpermute_b32 v1, v1, v68
	v_cvt_pk_bf16_f32 v66, v62, v63
	v_cvt_pk_bf16_f32 v67, v64, v65
	s_waitcnt lgkmcnt(0)
	v_add_f32_e32 v1, v68, v1
	v_fmamk_f32 v1, v1, 0x3a000000, v221
	v_mul_f32_e32 v68, 0x4f800000, v1
	v_cmp_gt_f32_e32 vcc, s71, v1
	s_nop 1
	v_cndmask_b32_e32 v1, v1, v68, vcc
	v_sqrt_f32_e32 v90, v1
	v_cvt_pk_bf16_f32 v68, v58, v59
	global_store_dwordx4 v[216:217], v[66:69], off offset:3072
	ds_write_b128 v226, v[62:65] offset:6144
	ds_write_b128 v226, v[58:61] offset:6160
	v_add_u32_e32 v66, -1, v90
	v_fma_f32 v67, -v66, v90, v1
	v_cmp_ge_f32_e64 s[6:7], 0, v67
	v_add_u32_e32 v67, 1, v90
	v_fma_f32 v68, -v67, v90, v1
	v_cndmask_b32_e64 v66, v90, v66, s[6:7]
	v_cmp_lt_f32_e64 s[6:7], 0, v68
	s_nop 1
	v_cndmask_b32_e64 v66, v66, v67, s[6:7]
	v_mul_f32_e32 v67, 0x37800000, v66
	v_cndmask_b32_e32 v66, v66, v67, vcc
	v_cmp_class_f32_e32 vcc, v1, v222
	s_nop 1
	v_cndmask_b32_e32 v1, v66, v1, vcc
	v_div_scale_f32 v66, s[6:7], v1, v1, 1.0
	v_rcp_f32_e32 v67, v66
	s_lshl_b64 s[6:7], s[62:63], 12
	v_lshl_add_u64 v[64:65], v[130:131], 0, s[6:7]
	v_fma_f32 v58, -v66, v67, 1.0
	v_fmac_f32_e32 v67, v58, v67
	v_div_scale_f32 v58, vcc, 1.0, v1, 1.0
	v_mul_f32_e32 v59, v58, v67
	v_fma_f32 v60, -v66, v59, v58
	v_fmac_f32_e32 v59, v60, v67
	v_fma_f32 v58, -v66, v59, v58
	v_div_fmas_f32 v58, v58, v67, v59
	v_div_fixup_f32 v62, v58, v1, 1.0
	v_pk_mul_f32 v[54:55], v[54:55], v[62:63] op_sel_hi:[1,0]
	v_pk_mul_f32 v[56:57], v[56:57], v[62:63] op_sel_hi:[1,0]
	v_pk_mul_f32 v[50:51], v[50:51], v[62:63] op_sel_hi:[1,0]
	v_pk_mul_f32 v[52:53], v[52:53], v[62:63] op_sel_hi:[1,0]
	v_pk_mul_f32 v[56:57], v[28:29], v[56:57]
	v_pk_mul_f32 v[54:55], v[26:27], v[54:55]
	v_pk_mul_f32 v[52:53], v[4:5], v[52:53]
	v_pk_mul_f32 v[50:51], v[2:3], v[50:51]
	v_pk_mul_f32 v[46:47], v[46:47], v[62:63] op_sel_hi:[1,0]
	v_pk_mul_f32 v[48:49], v[48:49], v[62:63] op_sel_hi:[1,0]
	v_pk_mul_f32 v[42:43], v[42:43], v[62:63] op_sel_hi:[1,0]
	v_pk_mul_f32 v[44:45], v[44:45], v[62:63] op_sel_hi:[1,0]
	v_cvt_pk_bf16_f32 v58, v54, v55
	v_cvt_pk_bf16_f32 v59, v56, v57
	v_cvt_pk_bf16_f32 v60, v50, v51
	v_cvt_pk_bf16_f32 v61, v52, v53
	v_add_u32_e32 v1, s34, v122
	v_pk_mul_f32 v[48:49], v[8:9], v[48:49]
	v_pk_mul_f32 v[46:47], v[6:7], v[46:47]
	v_pk_mul_f32 v[44:45], v[12:13], v[44:45]
	v_pk_mul_f32 v[42:43], v[10:11], v[42:43]
	v_pk_mul_f32 v[38:39], v[38:39], v[62:63] op_sel_hi:[1,0]
	v_pk_mul_f32 v[40:41], v[40:41], v[62:63] op_sel_hi:[1,0]
	v_pk_mul_f32 v[34:35], v[34:35], v[62:63] op_sel_hi:[1,0]
	v_pk_mul_f32 v[36:37], v[36:37], v[62:63] op_sel_hi:[1,0]
	global_store_dwordx4 v[64:65], v[58:61], off
	ds_write_b128 v1, v[54:57]
	ds_write_b128 v1, v[50:53] offset:16
	v_cvt_pk_bf16_f32 v50, v46, v47
	v_cvt_pk_bf16_f32 v51, v48, v49
	v_cvt_pk_bf16_f32 v52, v42, v43
	v_cvt_pk_bf16_f32 v53, v44, v45
	v_pk_mul_f32 v[40:41], v[20:21], v[40:41]
	v_pk_mul_f32 v[38:39], v[18:19], v[38:39]
	v_pk_mul_f32 v[36:37], v[16:17], v[36:37]
	v_pk_mul_f32 v[34:35], v[14:15], v[34:35]
	global_store_dwordx4 v[64:65], v[50:53], off offset:1024
	ds_write_b128 v1, v[46:49] offset:2048
	ds_write_b128 v1, v[42:45] offset:2064
	v_cvt_pk_bf16_f32 v42, v38, v39
	v_cvt_pk_bf16_f32 v43, v40, v41
	v_cvt_pk_bf16_f32 v44, v34, v35
	v_cvt_pk_bf16_f32 v45, v36, v37
	global_store_dwordx4 v[64:65], v[42:45], off offset:2048
	ds_write_b128 v1, v[38:41] offset:4096
	ds_write_b128 v1, v[34:37] offset:4112
	v_pk_mul_f32 v[34:35], v[102:103], v[62:63] op_sel_hi:[1,0]
	v_pk_mul_f32 v[36:37], v[104:105], v[62:63] op_sel_hi:[1,0]
	v_pk_mul_f32 v[38:39], v[98:99], v[62:63] op_sel_hi:[1,0]
	v_pk_mul_f32 v[40:41], v[100:101], v[62:63] op_sel_hi:[1,0]
	v_pk_mul_f32 v[36:37], v[24:25], v[36:37]
	v_pk_mul_f32 v[34:35], v[22:23], v[34:35]
	v_pk_mul_f32 v[40:41], v[32:33], v[40:41]
	v_pk_mul_f32 v[38:39], v[30:31], v[38:39]
	v_cvt_pk_bf16_f32 v42, v34, v35
	v_cvt_pk_bf16_f32 v43, v36, v37
	v_cvt_pk_bf16_f32 v44, v38, v39
	v_cvt_pk_bf16_f32 v45, v40, v41
	global_store_dwordx4 v[64:65], v[42:45], off offset:3072
	ds_write_b128 v1, v[34:37] offset:6144
	ds_write_b128 v1, v[38:41] offset:6160
	s_waitcnt lgkmcnt(0)
	s_barrier
	global_load_dwordx4 v[34:37], v[132:133], off
	global_load_dwordx4 v[38:41], v[134:135], off
	global_load_dwordx4 v[42:45], v[136:137], off
	global_load_dwordx4 v[46:49], v[138:139], off
	global_load_dwordx4 v[50:53], v[140:141], off
	global_load_dwordx4 v[54:57], v[142:143], off
	global_load_dwordx4 v[58:61], v[144:145], off
	global_load_dwordx4 v[62:65], v[146:147], off
	global_load_dwordx4 v[66:69], v[148:149], off
	global_load_dwordx4 v[90:93], v[150:151], off
	global_load_dwordx4 v[98:101], v[152:153], off
	global_load_dwordx4 v[102:105], v[154:155], off
	global_load_dwordx4 v[106:109], v[156:157], off
	global_load_dwordx4 v[110:113], v[158:159], off
	global_load_dwordx4 v[114:117], v[160:161], off
	global_load_dwordx4 v[118:121], v[162:163], off
	global_load_dwordx4 v[226:229], v[164:165], off
	global_load_dwordx4 v[230:233], v[166:167], off
	ds_read_b128 v[234:237], v123
	ds_read_b128 v[238:241], v123 offset:64
	s_waitcnt vmcnt(31) lgkmcnt(1)
	v_mfma_f32_16x16x4_f32 v[242:245], v234, v82, 0
	s_waitcnt vmcnt(30)
	v_mfma_f32_16x16x4_f32 v[246:249], v234, v86, 0
	s_waitcnt vmcnt(29)
	v_mfma_f32_16x16x4_f32 v[250:253], v234, v94, 0
	v_mfma_f32_16x16x4_f32 v[242:245], v235, v83, v[242:245]
	v_mfma_f32_16x16x4_f32 v[246:249], v235, v87, v[246:249]
	v_mfma_f32_16x16x4_f32 v[250:253], v235, v95, v[250:253]
	v_mfma_f32_16x16x4_f32 v[242:245], v236, v84, v[242:245]
	v_mfma_f32_16x16x4_f32 v[246:249], v236, v88, v[246:249]
	v_mfma_f32_16x16x4_f32 v[250:253], v236, v96, v[250:253]
	v_mfma_f32_16x16x4_f32 v[82:85], v237, v85, v[242:245]
	v_mfma_f32_16x16x4_f32 v[86:89], v237, v89, v[246:249]
	v_mfma_f32_16x16x4_f32 v[94:97], v237, v97, v[250:253]
	s_waitcnt vmcnt(28) lgkmcnt(0)
	v_mfma_f32_16x16x4_f32 v[82:85], v238, v70, v[82:85]
	s_waitcnt vmcnt(27)
	v_mfma_f32_16x16x4_f32 v[86:89], v238, v74, v[86:89]
	s_waitcnt vmcnt(26)
	v_mfma_f32_16x16x4_f32 v[94:97], v238, v78, v[94:97]
	v_mfma_f32_16x16x4_f32 v[82:85], v239, v71, v[82:85]
	v_mfma_f32_16x16x4_f32 v[86:89], v239, v75, v[86:89]
	v_mfma_f32_16x16x4_f32 v[94:97], v239, v79, v[94:97]
	v_mfma_f32_16x16x4_f32 v[82:85], v240, v72, v[82:85]
	v_mfma_f32_16x16x4_f32 v[86:89], v240, v76, v[86:89]
	v_mfma_f32_16x16x4_f32 v[94:97], v240, v80, v[94:97]
	v_mfma_f32_16x16x4_f32 v[70:73], v241, v73, v[82:85]
	v_mfma_f32_16x16x4_f32 v[74:77], v241, v77, v[86:89]
	s_nop 5
	ds_read_b128 v[82:85], v123 offset:128
	ds_read_b128 v[86:89], v123 offset:192
	v_mfma_f32_16x16x4_f32 v[78:81], v241, v81, v[94:97]
	s_waitcnt vmcnt(17) lgkmcnt(1)
	v_mfma_f32_16x16x4_f32 v[70:73], v82, v34, v[70:73]
	s_waitcnt vmcnt(16)
	v_mfma_f32_16x16x4_f32 v[74:77], v82, v38, v[74:77]
	s_waitcnt vmcnt(15)
	v_mfma_f32_16x16x4_f32 v[78:81], v82, v42, v[78:81]
	v_mfma_f32_16x16x4_f32 v[70:73], v83, v35, v[70:73]
	v_mfma_f32_16x16x4_f32 v[74:77], v83, v39, v[74:77]
	v_mfma_f32_16x16x4_f32 v[78:81], v83, v43, v[78:81]
	v_mfma_f32_16x16x4_f32 v[70:73], v84, v36, v[70:73]
	v_mfma_f32_16x16x4_f32 v[74:77], v84, v40, v[74:77]
	v_mfma_f32_16x16x4_f32 v[78:81], v84, v44, v[78:81]
	v_mfma_f32_16x16x4_f32 v[34:37], v85, v37, v[70:73]
	v_mfma_f32_16x16x4_f32 v[38:41], v85, v41, v[74:77]
	v_mfma_f32_16x16x4_f32 v[42:45], v85, v45, v[78:81]
	s_waitcnt vmcnt(12) lgkmcnt(0)
	v_mfma_f32_16x16x4_f32 v[42:45], v86, v54, v[42:45]
	v_mfma_f32_16x16x4_f32 v[34:37], v86, v46, v[34:37]
	v_mfma_f32_16x16x4_f32 v[38:41], v86, v50, v[38:41]
	v_mfma_f32_16x16x4_f32 v[42:45], v87, v55, v[42:45]
	v_mfma_f32_16x16x4_f32 v[34:37], v87, v47, v[34:37]
	v_mfma_f32_16x16x4_f32 v[38:41], v87, v51, v[38:41]
	v_mfma_f32_16x16x4_f32 v[42:45], v88, v56, v[42:45]
	v_mfma_f32_16x16x4_f32 v[34:37], v88, v48, v[34:37]
	v_mfma_f32_16x16x4_f32 v[38:41], v88, v52, v[38:41]
	v_mfma_f32_16x16x4_f32 v[34:37], v89, v49, v[34:37]
	global_load_dwordx4 v[46:49], v[168:169], off
	global_load_dwordx4 v[70:73], v[170:171], off
	global_load_dwordx4 v[74:77], v[172:173], off
	global_load_dwordx4 v[78:81], v[174:175], off
	v_mfma_f32_16x16x4_f32 v[38:41], v89, v53, v[38:41]
	global_load_dwordx4 v[50:53], v[176:177], off
	global_load_dwordx4 v[82:85], v[178:179], off
	global_load_dwordx4 v[94:97], v[180:181], off
	global_load_dwordx4 v[234:237], v[182:183], off
	global_load_dwordx4 v[238:241], v[184:185], off
	global_load_dwordx4 v[242:245], v[186:187], off
	global_load_dwordx4 v[246:249], v[188:189], off
	global_load_dwordx4 v[250:253], v[190:191], off
	v_mfma_f32_16x16x4_f32 v[42:45], v89, v57, v[42:45]
	ds_read_b128 v[54:57], v123 offset:256
	ds_read_b128 v[86:89], v123 offset:320
	s_waitcnt vmcnt(23) lgkmcnt(1)
	v_mfma_f32_16x16x4_f32 v[34:37], v54, v58, v[34:37]
	s_waitcnt vmcnt(22)
	v_mfma_f32_16x16x4_f32 v[38:41], v54, v62, v[38:41]
	s_waitcnt vmcnt(21)
	v_mfma_f32_16x16x4_f32 v[42:45], v54, v66, v[42:45]
	v_mfma_f32_16x16x4_f32 v[34:37], v55, v59, v[34:37]
	v_mfma_f32_16x16x4_f32 v[38:41], v55, v63, v[38:41]
	v_mfma_f32_16x16x4_f32 v[42:45], v55, v67, v[42:45]
	v_mfma_f32_16x16x4_f32 v[34:37], v56, v60, v[34:37]
	v_mfma_f32_16x16x4_f32 v[38:41], v56, v64, v[38:41]
	v_mfma_f32_16x16x4_f32 v[42:45], v56, v68, v[42:45]
	v_mfma_f32_16x16x4_f32 v[34:37], v57, v61, v[34:37]
	v_mfma_f32_16x16x4_f32 v[38:41], v57, v65, v[38:41]
	v_mfma_f32_16x16x4_f32 v[42:45], v57, v69, v[42:45]
	ds_read_b128 v[54:57], v123 offset:384
	ds_read_b128 v[58:61], v123 offset:448
	s_waitcnt vmcnt(20) lgkmcnt(2)
	v_mfma_f32_16x16x4_f32 v[34:37], v86, v90, v[34:37]
	s_waitcnt vmcnt(19)
	v_mfma_f32_16x16x4_f32 v[38:41], v86, v98, v[38:41]
	s_waitcnt vmcnt(18)
	v_mfma_f32_16x16x4_f32 v[42:45], v86, v102, v[42:45]
	v_mfma_f32_16x16x4_f32 v[34:37], v87, v91, v[34:37]
	v_mfma_f32_16x16x4_f32 v[38:41], v87, v99, v[38:41]
	v_mfma_f32_16x16x4_f32 v[42:45], v87, v103, v[42:45]
	v_mfma_f32_16x16x4_f32 v[34:37], v88, v92, v[34:37]
	v_mfma_f32_16x16x4_f32 v[38:41], v88, v100, v[38:41]
	v_mfma_f32_16x16x4_f32 v[42:45], v88, v104, v[42:45]
	v_mfma_f32_16x16x4_f32 v[34:37], v89, v93, v[34:37]
	v_mfma_f32_16x16x4_f32 v[38:41], v89, v101, v[38:41]
	v_mfma_f32_16x16x4_f32 v[42:45], v89, v105, v[42:45]
	s_waitcnt vmcnt(17) lgkmcnt(1)
	v_mfma_f32_16x16x4_f32 v[34:37], v54, v106, v[34:37]
	s_waitcnt vmcnt(16)
	v_mfma_f32_16x16x4_f32 v[38:41], v54, v110, v[38:41]
	s_waitcnt vmcnt(15)
	v_mfma_f32_16x16x4_f32 v[42:45], v54, v114, v[42:45]
	v_mfma_f32_16x16x4_f32 v[34:37], v55, v107, v[34:37]
	v_mfma_f32_16x16x4_f32 v[38:41], v55, v111, v[38:41]
	v_mfma_f32_16x16x4_f32 v[42:45], v55, v115, v[42:45]
	v_mfma_f32_16x16x4_f32 v[34:37], v56, v108, v[34:37]
	v_mfma_f32_16x16x4_f32 v[38:41], v56, v112, v[38:41]
	v_mfma_f32_16x16x4_f32 v[42:45], v56, v116, v[42:45]
	v_mfma_f32_16x16x4_f32 v[34:37], v57, v109, v[34:37]
	v_mfma_f32_16x16x4_f32 v[38:41], v57, v113, v[38:41]
	v_mfma_f32_16x16x4_f32 v[42:45], v57, v117, v[42:45]
	global_load_dwordx4 v[54:57], v[192:193], off
	global_load_dwordx4 v[62:65], v[194:195], off
	global_load_dwordx4 v[66:69], v[196:197], off
	global_load_dwordx4 v[86:89], v[198:199], off
	s_waitcnt vmcnt(16) lgkmcnt(0)
	v_mfma_f32_16x16x4_f32 v[42:45], v58, v230, v[42:45]
	v_mfma_f32_16x16x4_f32 v[34:37], v58, v118, v[34:37]
	v_mfma_f32_16x16x4_f32 v[38:41], v58, v226, v[38:41]
	v_mfma_f32_16x16x4_f32 v[42:45], v59, v231, v[42:45]
	v_mfma_f32_16x16x4_f32 v[34:37], v59, v119, v[34:37]
	v_mfma_f32_16x16x4_f32 v[38:41], v59, v227, v[38:41]
	v_mfma_f32_16x16x4_f32 v[42:45], v60, v232, v[42:45]
	v_mfma_f32_16x16x4_f32 v[34:37], v60, v120, v[34:37]
	v_mfma_f32_16x16x4_f32 v[38:41], v60, v228, v[38:41]
	v_mfma_f32_16x16x4_f32 v[34:37], v61, v121, v[34:37]
	v_mfma_f32_16x16x4_f32 v[38:41], v61, v229, v[38:41]
	global_load_dwordx4 v[90:93], v[200:201], off
	global_load_dwordx4 v[98:101], v[202:203], off
	global_load_dwordx4 v[102:105], v[204:205], off
	global_load_dwordx4 v[106:109], v[206:207], off
	global_load_dwordx4 v[110:113], v[208:209], off
	global_load_dwordx4 v[114:117], v[210:211], off
	global_load_dwordx4 v[118:121], v[212:213], off
	global_load_dwordx4 v[226:229], v[214:215], off
	v_mfma_f32_16x16x4_f32 v[42:45], v61, v233, v[42:45]
	ds_read_b128 v[58:61], v123 offset:512
	ds_read_b128 v[230:233], v123 offset:576
	s_waitcnt vmcnt(23) lgkmcnt(1)
	v_mfma_f32_16x16x4_f32 v[34:37], v58, v46, v[34:37]
	s_waitcnt vmcnt(22)
	v_mfma_f32_16x16x4_f32 v[38:41], v58, v70, v[38:41]
	s_waitcnt vmcnt(21)
	v_mfma_f32_16x16x4_f32 v[42:45], v58, v74, v[42:45]
	v_mfma_f32_16x16x4_f32 v[34:37], v59, v47, v[34:37]
	v_mfma_f32_16x16x4_f32 v[38:41], v59, v71, v[38:41]
	v_mfma_f32_16x16x4_f32 v[42:45], v59, v75, v[42:45]
	v_mfma_f32_16x16x4_f32 v[34:37], v60, v48, v[34:37]
	v_mfma_f32_16x16x4_f32 v[38:41], v60, v72, v[38:41]
	v_mfma_f32_16x16x4_f32 v[42:45], v60, v76, v[42:45]
	v_mfma_f32_16x16x4_f32 v[34:37], v61, v49, v[34:37]
	v_mfma_f32_16x16x4_f32 v[38:41], v61, v73, v[38:41]
	v_mfma_f32_16x16x4_f32 v[42:45], v61, v77, v[42:45]
	s_waitcnt vmcnt(20) lgkmcnt(0)
	v_mfma_f32_16x16x4_f32 v[34:37], v230, v78, v[34:37]
	s_waitcnt vmcnt(19)
	v_mfma_f32_16x16x4_f32 v[38:41], v230, v50, v[38:41]
	s_waitcnt vmcnt(18)
	v_mfma_f32_16x16x4_f32 v[42:45], v230, v82, v[42:45]
	v_mfma_f32_16x16x4_f32 v[34:37], v231, v79, v[34:37]
	v_mfma_f32_16x16x4_f32 v[38:41], v231, v51, v[38:41]
	v_mfma_f32_16x16x4_f32 v[42:45], v231, v83, v[42:45]
	v_mfma_f32_16x16x4_f32 v[34:37], v232, v80, v[34:37]
	v_mfma_f32_16x16x4_f32 v[38:41], v232, v52, v[38:41]
	v_mfma_f32_16x16x4_f32 v[42:45], v232, v84, v[42:45]
	v_mfma_f32_16x16x4_f32 v[34:37], v233, v81, v[34:37]
	v_mfma_f32_16x16x4_f32 v[38:41], v233, v53, v[38:41]
	ds_read_b128 v[46:49], v123 offset:640
	ds_read_b128 v[50:53], v123 offset:704
	v_mfma_f32_16x16x4_f32 v[42:45], v233, v85, v[42:45]
	s_waitcnt vmcnt(17) lgkmcnt(1)
	v_mfma_f32_16x16x4_f32 v[34:37], v46, v94, v[34:37]
	s_waitcnt vmcnt(16)
	v_mfma_f32_16x16x4_f32 v[38:41], v46, v234, v[38:41]
	s_waitcnt vmcnt(15)
	v_mfma_f32_16x16x4_f32 v[42:45], v46, v238, v[42:45]
	v_mfma_f32_16x16x4_f32 v[34:37], v47, v95, v[34:37]
	v_mfma_f32_16x16x4_f32 v[38:41], v47, v235, v[38:41]
	v_mfma_f32_16x16x4_f32 v[42:45], v47, v239, v[42:45]
	v_mfma_f32_16x16x4_f32 v[34:37], v48, v96, v[34:37]
	v_mfma_f32_16x16x4_f32 v[38:41], v48, v236, v[38:41]
	v_mfma_f32_16x16x4_f32 v[42:45], v48, v240, v[42:45]
	v_mfma_f32_16x16x4_f32 v[34:37], v49, v97, v[34:37]
	v_mfma_f32_16x16x4_f32 v[38:41], v49, v237, v[38:41]
	v_mfma_f32_16x16x4_f32 v[42:45], v49, v241, v[42:45]
	s_waitcnt vmcnt(14) lgkmcnt(0)
	v_mfma_f32_16x16x4_f32 v[34:37], v50, v242, v[34:37]
	s_waitcnt vmcnt(13)
	v_mfma_f32_16x16x4_f32 v[38:41], v50, v246, v[38:41]
	s_waitcnt vmcnt(12)
	v_mfma_f32_16x16x4_f32 v[42:45], v50, v250, v[42:45]
	v_mfma_f32_16x16x4_f32 v[34:37], v51, v243, v[34:37]
	v_mfma_f32_16x16x4_f32 v[38:41], v51, v247, v[38:41]
	v_mfma_f32_16x16x4_f32 v[42:45], v51, v251, v[42:45]
	v_mfma_f32_16x16x4_f32 v[34:37], v52, v244, v[34:37]
	v_mfma_f32_16x16x4_f32 v[38:41], v52, v248, v[38:41]
	v_mfma_f32_16x16x4_f32 v[42:45], v52, v252, v[42:45]
	v_mfma_f32_16x16x4_f32 v[34:37], v53, v245, v[34:37]
	v_mfma_f32_16x16x4_f32 v[38:41], v53, v249, v[38:41]
	v_mfma_f32_16x16x4_f32 v[42:45], v53, v253, v[42:45]
	ds_read_b128 v[46:49], v123 offset:768
	ds_read_b128 v[50:53], v123 offset:832
	s_waitcnt vmcnt(11) lgkmcnt(1)
	v_mfma_f32_16x16x4_f32 v[34:37], v46, v54, v[34:37]
	s_waitcnt vmcnt(10)
	v_mfma_f32_16x16x4_f32 v[38:41], v46, v62, v[38:41]
	s_waitcnt vmcnt(9)
	v_mfma_f32_16x16x4_f32 v[42:45], v46, v66, v[42:45]
	v_mfma_f32_16x16x4_f32 v[34:37], v47, v55, v[34:37]
	v_mfma_f32_16x16x4_f32 v[38:41], v47, v63, v[38:41]
	v_mfma_f32_16x16x4_f32 v[42:45], v47, v67, v[42:45]
	v_mfma_f32_16x16x4_f32 v[34:37], v48, v56, v[34:37]
	v_mfma_f32_16x16x4_f32 v[38:41], v48, v64, v[38:41]
	v_mfma_f32_16x16x4_f32 v[42:45], v48, v68, v[42:45]
	v_mfma_f32_16x16x4_f32 v[34:37], v49, v57, v[34:37]
	v_mfma_f32_16x16x4_f32 v[38:41], v49, v65, v[38:41]
	v_mfma_f32_16x16x4_f32 v[42:45], v49, v69, v[42:45]
	s_waitcnt vmcnt(8) lgkmcnt(0)
	v_mfma_f32_16x16x4_f32 v[34:37], v50, v86, v[34:37]
	s_waitcnt vmcnt(7)
	v_mfma_f32_16x16x4_f32 v[38:41], v50, v90, v[38:41]
	s_waitcnt vmcnt(6)
	v_mfma_f32_16x16x4_f32 v[42:45], v50, v98, v[42:45]
	v_mfma_f32_16x16x4_f32 v[34:37], v51, v87, v[34:37]
	v_mfma_f32_16x16x4_f32 v[38:41], v51, v91, v[38:41]
	v_mfma_f32_16x16x4_f32 v[42:45], v51, v99, v[42:45]
	v_mfma_f32_16x16x4_f32 v[34:37], v52, v88, v[34:37]
	v_mfma_f32_16x16x4_f32 v[38:41], v52, v92, v[38:41]
	v_mfma_f32_16x16x4_f32 v[42:45], v52, v100, v[42:45]
	v_mfma_f32_16x16x4_f32 v[34:37], v53, v89, v[34:37]
	v_mfma_f32_16x16x4_f32 v[38:41], v53, v93, v[38:41]
	v_mfma_f32_16x16x4_f32 v[42:45], v53, v101, v[42:45]
	ds_read_b128 v[46:49], v123 offset:896
	ds_read_b128 v[50:53], v123 offset:960
	s_waitcnt vmcnt(5) lgkmcnt(1)
	v_mfma_f32_16x16x4_f32 v[34:37], v46, v102, v[34:37]
	s_waitcnt vmcnt(4)
	v_mfma_f32_16x16x4_f32 v[38:41], v46, v106, v[38:41]
	s_waitcnt vmcnt(3)
	v_mfma_f32_16x16x4_f32 v[42:45], v46, v110, v[42:45]
	v_mfma_f32_16x16x4_f32 v[34:37], v47, v103, v[34:37]
	v_mfma_f32_16x16x4_f32 v[38:41], v47, v107, v[38:41]
	v_mfma_f32_16x16x4_f32 v[42:45], v47, v111, v[42:45]
	v_mfma_f32_16x16x4_f32 v[34:37], v48, v104, v[34:37]
	v_mfma_f32_16x16x4_f32 v[38:41], v48, v108, v[38:41]
	v_mfma_f32_16x16x4_f32 v[42:45], v48, v112, v[42:45]
	v_mfma_f32_16x16x4_f32 v[34:37], v49, v105, v[34:37]
	v_mfma_f32_16x16x4_f32 v[38:41], v49, v109, v[38:41]
	v_mfma_f32_16x16x4_f32 v[42:45], v49, v113, v[42:45]
	s_waitcnt vmcnt(2) lgkmcnt(0)
	v_mfma_f32_16x16x4_f32 v[34:37], v50, v114, v[34:37]
	s_waitcnt vmcnt(1)
	v_mfma_f32_16x16x4_f32 v[38:41], v50, v118, v[38:41]
	s_waitcnt vmcnt(0)
	v_mfma_f32_16x16x4_f32 v[42:45], v50, v226, v[42:45]
	v_mfma_f32_16x16x4_f32 v[34:37], v51, v115, v[34:37]
	v_mfma_f32_16x16x4_f32 v[38:41], v51, v119, v[38:41]
	v_mfma_f32_16x16x4_f32 v[42:45], v51, v227, v[42:45]
	v_mfma_f32_16x16x4_f32 v[34:37], v52, v116, v[34:37]
	v_mfma_f32_16x16x4_f32 v[38:41], v52, v120, v[38:41]
	v_mfma_f32_16x16x4_f32 v[42:45], v52, v228, v[42:45]
	v_mfma_f32_16x16x4_f32 v[34:37], v53, v117, v[34:37]
	v_mfma_f32_16x16x4_f32 v[38:41], v53, v121, v[38:41]
	v_mfma_f32_16x16x4_f32 v[42:45], v53, v229, v[42:45]
	s_cmp_gt_u32 s77, 2
	s_cbranch_scc1 .Lrpf_b_skip
	s_add_i32 s82, s77, 1
	s_lshl_b32 s82, s82, 4
	s_add_i32 s82, s76, s82
	s_ashr_i32 s83, s82, 31
	s_lshl_b64 s[82:83], s[82:83], 13
	v_lshl_add_u64 v[98:99], v[128:129], 0, s[82:83]
	s_add_u32 s82, s82, 0x1000
	s_addc_u32 s83, s83, 0
	global_load_dwordx4 v[118:121], v[98:99], off
	global_load_dwordx4 v[114:117], v[98:99], off offset:16
	global_load_dwordx4 v[110:113], v[98:99], off offset:2048
	global_load_dwordx4 v[106:109], v[98:99], off offset:2064
	v_lshl_add_u64 v[100:101], v[128:129], 0, s[82:83]
	s_add_u32 s82, s82, 0x1000
	s_addc_u32 s83, s83, 0
	global_load_dwordx4 v[58:61], v[100:101], off offset:2064
	global_load_dwordx4 v[90:93], v[100:101], off
	global_load_dwordx4 v[66:69], v[100:101], off offset:16
	global_load_dwordx4 v[62:65], v[100:101], off offset:2048
	v_lshl_add_u64 v[98:99], v[128:129], 0, s[82:83]
	s_nop 0
	global_load_dwordx4 v[54:57], v[98:99], off
	global_load_dwordx4 v[50:53], v[98:99], off offset:16
	global_load_dwordx4 v[234:237], v[98:99], off offset:2064
	global_load_dwordx4 v[238:241], v[98:99], off offset:2048
	s_add_u32 s82, s82, 0x1000
	s_addc_u32 s83, s83, 0
	v_lshl_add_u64 v[100:101], v[128:129], 0, s[82:83]
	s_nop 0
	global_load_dwordx4 v[242:245], v[100:101], off
	global_load_dwordx4 v[246:249], v[100:101], off offset:16
	global_load_dwordx4 v[102:105], v[100:101], off offset:2048
	global_load_dwordx4 v[250:253], v[100:101], off offset:2064
